# P2 row phase rewritten by hand: per-thread 8 consecutive tokens, sliding causal-window sums + conv products formed once per row (f32 math as before, bf16 storage as before)
# baseline (speedup 1.0000x reference)
.LBB0_376:
	s_or_b64 exec, exec, s[6:7]
	s_cmp_lt_i32 s94, 3
	s_cselect_b64 s[0:1], -1, 0
	s_and_b64 s[56:57], s[0:1], s[4:5]
	s_andn2_b64 vcc, exec, s[56:57]
	s_cbranch_vccnz .LBB0_387
	s_add_u32 s62, s90, 0x21100000
	s_addc_u32 s63, s91, 0
	s_add_u32 s76, s90, 0x8100000
	s_addc_u32 s77, s91, 0
	s_waitcnt vmcnt(0)
	v_readlane_b32 s7, v255, 0
	v_readlane_b32 s1, v255, 4
	v_mbcnt_lo_u32_b32 v0, -1, 0
	v_mbcnt_hi_u32_b32 v0, -1, v0
	s_lshr_b32 s0, s7, 7
	s_lshl_b32 s4, s1, 5
	s_lshl_b32 s0, s0, 3
	s_add_i32 s4, s4, s0
	s_and_b32 s5, s4, 0x7ff
	s_sub_i32 s0, s4, s5
	s_lshl_b32 s0, s0, 14
	s_add_u32 s22, s62, s0
	s_addc_u32 s23, s63, 0
	s_lshl_b32 s0, s4, 14
	s_add_u32 s24, s62, s0
	s_addc_u32 s25, s63, 0
	s_lshl_b32 s0, s4, 12
	s_add_u32 s26, s76, s0
	s_addc_u32 s27, s77, 0
	s_mov_b32 s8, 0
	s_mov_b32 s9, -1
	s_and_b32 s0, s7, 64
	v_or_b32_e32 v0, s0, v0
	v_lshlrev_b32_e32 v220, 4, v0
	v_add_u32_e32 v221, 0x1000, v220
	v_lshlrev_b32_e32 v217, 5, v0
	s_bitcmp0_b32 s7, 6
	s_cbranch_scc1 .Lp2_even
	s_add_i32 s2, s5, -15
	s_max_i32 s2, s2, 0
	s_lshl_b32 s2, s2, 14
	s_add_u32 s20, s22, s2
	s_addc_u32 s21, s23, 0
	global_load_dwordx4 v[0:3], v220, s[20:21]
	s_add_i32 s2, s5, -14
	s_max_i32 s2, s2, 0
	s_lshl_b32 s2, s2, 14
	s_add_u32 s20, s22, s2
	s_addc_u32 s21, s23, 0
	global_load_dwordx4 v[4:7], v220, s[20:21]
	s_add_i32 s2, s5, -13
	s_max_i32 s2, s2, 0
	s_lshl_b32 s2, s2, 14
	s_add_u32 s20, s22, s2
	s_addc_u32 s21, s23, 0
	global_load_dwordx4 v[8:11], v220, s[20:21]
	s_add_i32 s2, s5, -12
	s_max_i32 s2, s2, 0
	s_lshl_b32 s2, s2, 14
	s_add_u32 s20, s22, s2
	s_addc_u32 s21, s23, 0
	global_load_dwordx4 v[12:15], v220, s[20:21]
	s_add_i32 s2, s5, -11
	s_max_i32 s2, s2, 0
	s_lshl_b32 s2, s2, 14
	s_add_u32 s20, s22, s2
	s_addc_u32 s21, s23, 0
	global_load_dwordx4 v[16:19], v220, s[20:21]
	s_add_i32 s2, s5, -10
	s_max_i32 s2, s2, 0
	s_lshl_b32 s2, s2, 14
	s_add_u32 s20, s22, s2
	s_addc_u32 s21, s23, 0
	global_load_dwordx4 v[20:23], v220, s[20:21]
	s_add_i32 s2, s5, -9
	s_max_i32 s2, s2, 0
	s_lshl_b32 s2, s2, 14
	s_add_u32 s20, s22, s2
	s_addc_u32 s21, s23, 0
	global_load_dwordx4 v[24:27], v220, s[20:21]
	s_add_i32 s2, s5, -8
	s_max_i32 s2, s2, 0
	s_lshl_b32 s2, s2, 14
	s_add_u32 s20, s22, s2
	s_addc_u32 s21, s23, 0
	global_load_dwordx4 v[28:31], v220, s[20:21]
	s_add_i32 s2, s5, -7
	s_max_i32 s2, s2, 0
	s_lshl_b32 s2, s2, 14
	s_add_u32 s20, s22, s2
	s_addc_u32 s21, s23, 0
	global_load_dwordx4 v[32:35], v220, s[20:21]
	s_add_i32 s2, s5, -6
	s_max_i32 s2, s2, 0
	s_lshl_b32 s2, s2, 14
	s_add_u32 s20, s22, s2
	s_addc_u32 s21, s23, 0
	global_load_dwordx4 v[36:39], v220, s[20:21]
	s_add_i32 s2, s5, -5
	s_max_i32 s2, s2, 0
	s_lshl_b32 s2, s2, 14
	s_add_u32 s20, s22, s2
	s_addc_u32 s21, s23, 0
	global_load_dwordx4 v[40:43], v220, s[20:21]
	s_add_i32 s2, s5, -4
	s_max_i32 s2, s2, 0
	s_lshl_b32 s2, s2, 14
	s_add_u32 s20, s22, s2
	s_addc_u32 s21, s23, 0
	global_load_dwordx4 v[44:47], v220, s[20:21]
	s_add_i32 s2, s5, -3
	s_max_i32 s2, s2, 0
	s_lshl_b32 s2, s2, 14
	s_add_u32 s20, s22, s2
	s_addc_u32 s21, s23, 0
	global_load_dwordx4 v[48:51], v220, s[20:21]
	s_add_i32 s2, s5, -2
	s_max_i32 s2, s2, 0
	s_lshl_b32 s2, s2, 14
	s_add_u32 s20, s22, s2
	s_addc_u32 s21, s23, 0
	global_load_dwordx4 v[52:55], v220, s[20:21]
	s_add_i32 s2, s5, -1
	s_max_i32 s2, s2, 0
	s_lshl_b32 s2, s2, 14
	s_add_u32 s20, s22, s2
	s_addc_u32 s21, s23, 0
	global_load_dwordx4 v[56:59], v220, s[20:21]
	global_load_dwordx4 v[60:63], v220, s[24:25]
	s_add_u32 s20, s24, 0x4000
	s_addc_u32 s21, s25, 0
	global_load_dwordx4 v[64:67], v220, s[20:21]
	s_add_u32 s20, s24, 0x8000
	s_addc_u32 s21, s25, 0
	global_load_dwordx4 v[68:71], v220, s[20:21]
	s_add_u32 s20, s24, 0xc000
	s_addc_u32 s21, s25, 0
	global_load_dwordx4 v[72:75], v220, s[20:21]
	s_add_u32 s20, s24, 0x10000
	s_addc_u32 s21, s25, 0
	global_load_dwordx4 v[76:79], v220, s[20:21]
	s_add_u32 s20, s24, 0x14000
	s_addc_u32 s21, s25, 0
	global_load_dwordx4 v[80:83], v220, s[20:21]
	s_add_u32 s20, s24, 0x18000
	s_addc_u32 s21, s25, 0
	global_load_dwordx4 v[84:87], v220, s[20:21]
	s_add_u32 s20, s24, 0x1c000
	s_addc_u32 s21, s25, 0
	global_load_dwordx4 v[88:91], v220, s[20:21]
	global_load_dwordx4 v[92:95], v217, s[82:83]
	global_load_dwordx4 v[96:99], v217, s[82:83] offset:16
	s_add_u32 s20, s82, 0x1000
	s_addc_u32 s21, s83, 0
	global_load_dwordx4 v[100:103], v217, s[20:21]
	global_load_dwordx4 v[104:107], v217, s[20:21] offset:16
	s_add_u32 s20, s82, 0x2000
	s_addc_u32 s21, s83, 0
	global_load_dwordx4 v[108:111], v217, s[20:21]
	global_load_dwordx4 v[112:115], v217, s[20:21] offset:16
	global_load_dwordx4 v[116:119], v220, s[24:25] offset:2048
	s_add_u32 s20, s24, 0x4000
	s_addc_u32 s21, s25, 0
	global_load_dwordx4 v[120:123], v220, s[20:21] offset:2048
	s_add_u32 s20, s24, 0x8000
	s_addc_u32 s21, s25, 0
	global_load_dwordx4 v[124:127], v220, s[20:21] offset:2048
	s_add_u32 s20, s24, 0xc000
	s_addc_u32 s21, s25, 0
	global_load_dwordx4 v[128:131], v220, s[20:21] offset:2048
	s_add_u32 s20, s24, 0x10000
	s_addc_u32 s21, s25, 0
	global_load_dwordx4 v[132:135], v220, s[20:21] offset:2048
	s_add_u32 s20, s24, 0x14000
	s_addc_u32 s21, s25, 0
	global_load_dwordx4 v[136:139], v220, s[20:21] offset:2048
	s_add_u32 s20, s24, 0x18000
	s_addc_u32 s21, s25, 0
	global_load_dwordx4 v[140:143], v220, s[20:21] offset:2048
	s_add_u32 s20, s24, 0x1c000
	s_addc_u32 s21, s25, 0
	global_load_dwordx4 v[144:147], v220, s[20:21] offset:2048
	s_add_i32 s2, s5, -2
	s_max_i32 s2, s2, 0
	s_lshl_b32 s2, s2, 14
	s_add_u32 s20, s22, s2
	s_addc_u32 s21, s23, 0
	global_load_dwordx4 v[148:151], v221, s[20:21]
	global_load_dwordx4 v[152:155], v221, s[20:21] offset:2048
	s_add_i32 s2, s5, -1
	s_max_i32 s2, s2, 0
	s_lshl_b32 s2, s2, 14
	s_add_u32 s20, s22, s2
	s_addc_u32 s21, s23, 0
	global_load_dwordx4 v[156:159], v221, s[20:21]
	global_load_dwordx4 v[160:163], v221, s[20:21] offset:2048
	global_load_dwordx4 v[164:167], v221, s[24:25]
	global_load_dwordx4 v[168:171], v221, s[24:25] offset:2048
	s_add_u32 s20, s24, 0x4000
	s_addc_u32 s21, s25, 0
	global_load_dwordx4 v[172:175], v221, s[20:21]
	global_load_dwordx4 v[176:179], v221, s[20:21] offset:2048
	v_cndmask_b32_e64 v219, 8, 16, s[8:9]
	v_cndmask_b32_e64 v218, 0, 1.0, s[8:9]
	s_cmp_ge_u32 s5, 15
	s_cbranch_scc1 .Lp2_nomask_odd
	s_waitcnt vmcnt(30)
	s_add_i32 s2, s5, -15
	s_cmp_lt_i32 s2, 0
	s_cselect_b32 s2, 0, -1
	v_and_b32_e32 v0, s2, v0
	v_and_b32_e32 v1, s2, v1
	v_and_b32_e32 v2, s2, v2
	v_and_b32_e32 v3, s2, v3
	s_add_i32 s2, s5, -14
	s_cmp_lt_i32 s2, 0
	s_cselect_b32 s2, 0, -1
	v_and_b32_e32 v4, s2, v4
	v_and_b32_e32 v5, s2, v5
	v_and_b32_e32 v6, s2, v6
	v_and_b32_e32 v7, s2, v7
	s_add_i32 s2, s5, -13
	s_cmp_lt_i32 s2, 0
	s_cselect_b32 s2, 0, -1
	v_and_b32_e32 v8, s2, v8
	v_and_b32_e32 v9, s2, v9
	v_and_b32_e32 v10, s2, v10
	v_and_b32_e32 v11, s2, v11
	s_add_i32 s2, s5, -12
	s_cmp_lt_i32 s2, 0
	s_cselect_b32 s2, 0, -1
	v_and_b32_e32 v12, s2, v12
	v_and_b32_e32 v13, s2, v13
	v_and_b32_e32 v14, s2, v14
	v_and_b32_e32 v15, s2, v15
	s_add_i32 s2, s5, -11
	s_cmp_lt_i32 s2, 0
	s_cselect_b32 s2, 0, -1
	v_and_b32_e32 v16, s2, v16
	v_and_b32_e32 v17, s2, v17
	v_and_b32_e32 v18, s2, v18
	v_and_b32_e32 v19, s2, v19
	s_add_i32 s2, s5, -10
	s_cmp_lt_i32 s2, 0
	s_cselect_b32 s2, 0, -1
	v_and_b32_e32 v20, s2, v20
	v_and_b32_e32 v21, s2, v21
	v_and_b32_e32 v22, s2, v22
	v_and_b32_e32 v23, s2, v23
	s_add_i32 s2, s5, -9
	s_cmp_lt_i32 s2, 0
	s_cselect_b32 s2, 0, -1
	v_and_b32_e32 v24, s2, v24
	v_and_b32_e32 v25, s2, v25
	v_and_b32_e32 v26, s2, v26
	v_and_b32_e32 v27, s2, v27
	s_add_i32 s2, s5, -8
	s_cmp_lt_i32 s2, 0
	s_cselect_b32 s2, 0, -1
	v_and_b32_e32 v28, s2, v28
	v_and_b32_e32 v29, s2, v29
	v_and_b32_e32 v30, s2, v30
	v_and_b32_e32 v31, s2, v31
	s_add_i32 s2, s5, -7
	s_cmp_lt_i32 s2, 0
	s_cselect_b32 s2, 0, -1
	v_and_b32_e32 v32, s2, v32
	v_and_b32_e32 v33, s2, v33
	v_and_b32_e32 v34, s2, v34
	v_and_b32_e32 v35, s2, v35
	s_add_i32 s2, s5, -6
	s_cmp_lt_i32 s2, 0
	s_cselect_b32 s2, 0, -1
	v_and_b32_e32 v36, s2, v36
	v_and_b32_e32 v37, s2, v37
	v_and_b32_e32 v38, s2, v38
	v_and_b32_e32 v39, s2, v39
	s_add_i32 s2, s5, -5
	s_cmp_lt_i32 s2, 0
	s_cselect_b32 s2, 0, -1
	v_and_b32_e32 v40, s2, v40
	v_and_b32_e32 v41, s2, v41
	v_and_b32_e32 v42, s2, v42
	v_and_b32_e32 v43, s2, v43
	s_add_i32 s2, s5, -4
	s_cmp_lt_i32 s2, 0
	s_cselect_b32 s2, 0, -1
	v_and_b32_e32 v44, s2, v44
	v_and_b32_e32 v45, s2, v45
	v_and_b32_e32 v46, s2, v46
	v_and_b32_e32 v47, s2, v47
	s_add_i32 s2, s5, -3
	s_cmp_lt_i32 s2, 0
	s_cselect_b32 s2, 0, -1
	v_and_b32_e32 v48, s2, v48
	v_and_b32_e32 v49, s2, v49
	v_and_b32_e32 v50, s2, v50
	v_and_b32_e32 v51, s2, v51
	s_add_i32 s2, s5, -2
	s_cmp_lt_i32 s2, 0
	s_cselect_b32 s2, 0, -1
	v_and_b32_e32 v52, s2, v52
	v_and_b32_e32 v53, s2, v53
	v_and_b32_e32 v54, s2, v54
	v_and_b32_e32 v55, s2, v55
	s_add_i32 s2, s5, -1
	s_cmp_lt_i32 s2, 0
	s_cselect_b32 s2, 0, -1
	v_and_b32_e32 v56, s2, v56
	v_and_b32_e32 v57, s2, v57
	v_and_b32_e32 v58, s2, v58
	v_and_b32_e32 v59, s2, v59
.Lp2_nomask_odd:
	s_waitcnt vmcnt(44)
	v_lshlrev_b32_e32 v196, 16, v0
	v_and_b32_e32 v197, 0xffff0000, v0
	v_lshlrev_b32_e32 v198, 16, v1
	v_and_b32_e32 v199, 0xffff0000, v1
	v_lshlrev_b32_e32 v200, 16, v2
	v_and_b32_e32 v201, 0xffff0000, v2
	v_lshlrev_b32_e32 v202, 16, v3
	v_and_b32_e32 v203, 0xffff0000, v3
	s_waitcnt vmcnt(43)
	v_lshlrev_b32_e32 v188, 16, v4
	v_and_b32_e32 v189, 0xffff0000, v4
	v_lshlrev_b32_e32 v190, 16, v5
	v_and_b32_e32 v191, 0xffff0000, v5
	v_lshlrev_b32_e32 v192, 16, v6
	v_and_b32_e32 v193, 0xffff0000, v6
	v_lshlrev_b32_e32 v194, 16, v7
	v_and_b32_e32 v195, 0xffff0000, v7
	v_pk_add_f32 v[196:197], v[196:197], v[188:189]
	v_pk_add_f32 v[198:199], v[198:199], v[190:191]
	v_pk_add_f32 v[200:201], v[200:201], v[192:193]
	v_pk_add_f32 v[202:203], v[202:203], v[194:195]
	s_waitcnt vmcnt(42)
	v_lshlrev_b32_e32 v188, 16, v8
	v_and_b32_e32 v189, 0xffff0000, v8
	v_lshlrev_b32_e32 v190, 16, v9
	v_and_b32_e32 v191, 0xffff0000, v9
	v_lshlrev_b32_e32 v192, 16, v10
	v_and_b32_e32 v193, 0xffff0000, v10
	v_lshlrev_b32_e32 v194, 16, v11
	v_and_b32_e32 v195, 0xffff0000, v11
	v_pk_add_f32 v[196:197], v[196:197], v[188:189]
	v_pk_add_f32 v[198:199], v[198:199], v[190:191]
	v_pk_add_f32 v[200:201], v[200:201], v[192:193]
	v_pk_add_f32 v[202:203], v[202:203], v[194:195]
	s_waitcnt vmcnt(41)
	v_lshlrev_b32_e32 v188, 16, v12
	v_and_b32_e32 v189, 0xffff0000, v12
	v_lshlrev_b32_e32 v190, 16, v13
	v_and_b32_e32 v191, 0xffff0000, v13
	v_lshlrev_b32_e32 v192, 16, v14
	v_and_b32_e32 v193, 0xffff0000, v14
	v_lshlrev_b32_e32 v194, 16, v15
	v_and_b32_e32 v195, 0xffff0000, v15
	v_pk_add_f32 v[196:197], v[196:197], v[188:189]
	v_pk_add_f32 v[198:199], v[198:199], v[190:191]
	v_pk_add_f32 v[200:201], v[200:201], v[192:193]
	v_pk_add_f32 v[202:203], v[202:203], v[194:195]
	s_waitcnt vmcnt(40)
	v_lshlrev_b32_e32 v188, 16, v16
	v_and_b32_e32 v189, 0xffff0000, v16
	v_lshlrev_b32_e32 v190, 16, v17
	v_and_b32_e32 v191, 0xffff0000, v17
	v_lshlrev_b32_e32 v192, 16, v18
	v_and_b32_e32 v193, 0xffff0000, v18
	v_lshlrev_b32_e32 v194, 16, v19
	v_and_b32_e32 v195, 0xffff0000, v19
	v_pk_add_f32 v[196:197], v[196:197], v[188:189]
	v_pk_add_f32 v[198:199], v[198:199], v[190:191]
	v_pk_add_f32 v[200:201], v[200:201], v[192:193]
	v_pk_add_f32 v[202:203], v[202:203], v[194:195]
	s_waitcnt vmcnt(39)
	v_lshlrev_b32_e32 v188, 16, v20
	v_and_b32_e32 v189, 0xffff0000, v20
	v_lshlrev_b32_e32 v190, 16, v21
	v_and_b32_e32 v191, 0xffff0000, v21
	v_lshlrev_b32_e32 v192, 16, v22
	v_and_b32_e32 v193, 0xffff0000, v22
	v_lshlrev_b32_e32 v194, 16, v23
	v_and_b32_e32 v195, 0xffff0000, v23
	v_pk_add_f32 v[196:197], v[196:197], v[188:189]
	v_pk_add_f32 v[198:199], v[198:199], v[190:191]
	v_pk_add_f32 v[200:201], v[200:201], v[192:193]
	v_pk_add_f32 v[202:203], v[202:203], v[194:195]
	s_waitcnt vmcnt(38)
	v_lshlrev_b32_e32 v188, 16, v24
	v_and_b32_e32 v189, 0xffff0000, v24
	v_lshlrev_b32_e32 v190, 16, v25
	v_and_b32_e32 v191, 0xffff0000, v25
	v_lshlrev_b32_e32 v192, 16, v26
	v_and_b32_e32 v193, 0xffff0000, v26
	v_lshlrev_b32_e32 v194, 16, v27
	v_and_b32_e32 v195, 0xffff0000, v27
	v_pk_add_f32 v[196:197], v[196:197], v[188:189]
	v_pk_add_f32 v[198:199], v[198:199], v[190:191]
	v_pk_add_f32 v[200:201], v[200:201], v[192:193]
	v_pk_add_f32 v[202:203], v[202:203], v[194:195]
	s_waitcnt vmcnt(37)
	v_lshlrev_b32_e32 v188, 16, v28
	v_and_b32_e32 v189, 0xffff0000, v28
	v_lshlrev_b32_e32 v190, 16, v29
	v_and_b32_e32 v191, 0xffff0000, v29
	v_lshlrev_b32_e32 v192, 16, v30
	v_and_b32_e32 v193, 0xffff0000, v30
	v_lshlrev_b32_e32 v194, 16, v31
	v_and_b32_e32 v195, 0xffff0000, v31
	v_pk_add_f32 v[196:197], v[196:197], v[188:189]
	v_pk_add_f32 v[198:199], v[198:199], v[190:191]
	v_pk_add_f32 v[200:201], v[200:201], v[192:193]
	v_pk_add_f32 v[202:203], v[202:203], v[194:195]
	s_waitcnt vmcnt(36)
	v_lshlrev_b32_e32 v180, 16, v32
	v_and_b32_e32 v181, 0xffff0000, v32
	v_lshlrev_b32_e32 v182, 16, v33
	v_and_b32_e32 v183, 0xffff0000, v33
	v_lshlrev_b32_e32 v184, 16, v34
	v_and_b32_e32 v185, 0xffff0000, v34
	v_lshlrev_b32_e32 v186, 16, v35
	v_and_b32_e32 v187, 0xffff0000, v35
	s_waitcnt vmcnt(35)
	v_lshlrev_b32_e32 v188, 16, v36
	v_and_b32_e32 v189, 0xffff0000, v36
	v_lshlrev_b32_e32 v190, 16, v37
	v_and_b32_e32 v191, 0xffff0000, v37
	v_lshlrev_b32_e32 v192, 16, v38
	v_and_b32_e32 v193, 0xffff0000, v38
	v_lshlrev_b32_e32 v194, 16, v39
	v_and_b32_e32 v195, 0xffff0000, v39
	v_pk_add_f32 v[180:181], v[180:181], v[188:189]
	v_pk_add_f32 v[182:183], v[182:183], v[190:191]
	v_pk_add_f32 v[184:185], v[184:185], v[192:193]
	v_pk_add_f32 v[186:187], v[186:187], v[194:195]
	s_waitcnt vmcnt(34)
	v_lshlrev_b32_e32 v188, 16, v40
	v_and_b32_e32 v189, 0xffff0000, v40
	v_lshlrev_b32_e32 v190, 16, v41
	v_and_b32_e32 v191, 0xffff0000, v41
	v_lshlrev_b32_e32 v192, 16, v42
	v_and_b32_e32 v193, 0xffff0000, v42
	v_lshlrev_b32_e32 v194, 16, v43
	v_and_b32_e32 v195, 0xffff0000, v43
	v_pk_add_f32 v[180:181], v[180:181], v[188:189]
	v_pk_add_f32 v[182:183], v[182:183], v[190:191]
	v_pk_add_f32 v[184:185], v[184:185], v[192:193]
	v_pk_add_f32 v[186:187], v[186:187], v[194:195]
	s_waitcnt vmcnt(33)
	v_lshlrev_b32_e32 v188, 16, v44
	v_and_b32_e32 v189, 0xffff0000, v44
	v_lshlrev_b32_e32 v190, 16, v45
	v_and_b32_e32 v191, 0xffff0000, v45
	v_lshlrev_b32_e32 v192, 16, v46
	v_and_b32_e32 v193, 0xffff0000, v46
	v_lshlrev_b32_e32 v194, 16, v47
	v_and_b32_e32 v195, 0xffff0000, v47
	v_pk_add_f32 v[180:181], v[180:181], v[188:189]
	v_pk_add_f32 v[182:183], v[182:183], v[190:191]
	v_pk_add_f32 v[184:185], v[184:185], v[192:193]
	v_pk_add_f32 v[186:187], v[186:187], v[194:195]
	s_waitcnt vmcnt(32)
	v_lshlrev_b32_e32 v188, 16, v48
	v_and_b32_e32 v189, 0xffff0000, v48
	v_lshlrev_b32_e32 v190, 16, v49
	v_and_b32_e32 v191, 0xffff0000, v49
	v_lshlrev_b32_e32 v192, 16, v50
	v_and_b32_e32 v193, 0xffff0000, v50
	v_lshlrev_b32_e32 v194, 16, v51
	v_and_b32_e32 v195, 0xffff0000, v51
	v_pk_add_f32 v[180:181], v[180:181], v[188:189]
	v_pk_add_f32 v[182:183], v[182:183], v[190:191]
	v_pk_add_f32 v[184:185], v[184:185], v[192:193]
	v_pk_add_f32 v[186:187], v[186:187], v[194:195]
	s_waitcnt vmcnt(31)
	v_lshlrev_b32_e32 v188, 16, v52
	v_and_b32_e32 v189, 0xffff0000, v52
	v_lshlrev_b32_e32 v190, 16, v53
	v_and_b32_e32 v191, 0xffff0000, v53
	v_lshlrev_b32_e32 v192, 16, v54
	v_and_b32_e32 v193, 0xffff0000, v54
	v_lshlrev_b32_e32 v194, 16, v55
	v_and_b32_e32 v195, 0xffff0000, v55
	v_pk_add_f32 v[180:181], v[180:181], v[188:189]
	v_pk_add_f32 v[182:183], v[182:183], v[190:191]
	v_pk_add_f32 v[184:185], v[184:185], v[192:193]
	v_pk_add_f32 v[186:187], v[186:187], v[194:195]
	s_waitcnt vmcnt(30)
	v_lshlrev_b32_e32 v188, 16, v56
	v_and_b32_e32 v189, 0xffff0000, v56
	v_lshlrev_b32_e32 v190, 16, v57
	v_and_b32_e32 v191, 0xffff0000, v57
	v_lshlrev_b32_e32 v192, 16, v58
	v_and_b32_e32 v193, 0xffff0000, v58
	v_lshlrev_b32_e32 v194, 16, v59
	v_and_b32_e32 v195, 0xffff0000, v59
	v_pk_add_f32 v[180:181], v[180:181], v[188:189]
	v_pk_add_f32 v[182:183], v[182:183], v[190:191]
	v_pk_add_f32 v[184:185], v[184:185], v[192:193]
	v_pk_add_f32 v[186:187], v[186:187], v[194:195]
	v_pk_fma_f32 v[180:181], v[196:197], v[218:219], v[180:181] op_sel_hi:[1,0,1]
	v_pk_fma_f32 v[182:183], v[198:199], v[218:219], v[182:183] op_sel_hi:[1,0,1]
	v_pk_fma_f32 v[184:185], v[200:201], v[218:219], v[184:185] op_sel_hi:[1,0,1]
	v_pk_fma_f32 v[186:187], v[202:203], v[218:219], v[186:187] op_sel_hi:[1,0,1]
	s_add_i32 s2, s5, 1
	v_min_u32_e32 v217, s2, v219
	v_cvt_f32_u32_e32 v217, v217
	v_rcp_f32_e32 v216, v217
	s_waitcnt vmcnt(29)
	v_lshlrev_b32_e32 v188, 16, v60
	v_and_b32_e32 v189, 0xffff0000, v60
	v_lshlrev_b32_e32 v190, 16, v61
	v_and_b32_e32 v191, 0xffff0000, v61
	v_lshlrev_b32_e32 v192, 16, v62
	v_and_b32_e32 v193, 0xffff0000, v62
	v_lshlrev_b32_e32 v194, 16, v63
	v_and_b32_e32 v195, 0xffff0000, v63
	v_pk_add_f32 v[180:181], v[180:181], v[188:189]
	v_pk_add_f32 v[182:183], v[182:183], v[190:191]
	v_pk_add_f32 v[184:185], v[184:185], v[192:193]
	v_pk_add_f32 v[186:187], v[186:187], v[194:195]
	v_pk_fma_f32 v[196:197], v[180:181], v[216:217], v[188:189] op_sel_hi:[1,0,1] neg_lo:[0,0,1] neg_hi:[0,0,1]
	v_pk_fma_f32 v[198:199], v[182:183], v[216:217], v[190:191] op_sel_hi:[1,0,1] neg_lo:[0,0,1] neg_hi:[0,0,1]
	v_pk_fma_f32 v[200:201], v[184:185], v[216:217], v[192:193] op_sel_hi:[1,0,1] neg_lo:[0,0,1] neg_hi:[0,0,1]
	v_pk_fma_f32 v[202:203], v[186:187], v[216:217], v[194:195] op_sel_hi:[1,0,1] neg_lo:[0,0,1] neg_hi:[0,0,1]
	v_cvt_pk_bf16_f32 v208, v196, v197
	v_cvt_pk_bf16_f32 v209, v198, v199
	v_cvt_pk_bf16_f32 v210, v200, v201
	v_cvt_pk_bf16_f32 v211, v202, v203
	global_store_dwordx4 v220, v[208:211], s[26:27]
	v_cndmask_b32_e64 v204, v32, v0, s[8:9]
	v_cndmask_b32_e64 v205, v33, v1, s[8:9]
	v_cndmask_b32_e64 v206, v34, v2, s[8:9]
	v_cndmask_b32_e64 v207, v35, v3, s[8:9]
	v_lshlrev_b32_e32 v196, 16, v204
	v_and_b32_e32 v197, 0xffff0000, v204
	v_lshlrev_b32_e32 v198, 16, v205
	v_and_b32_e32 v199, 0xffff0000, v205
	v_lshlrev_b32_e32 v200, 16, v206
	v_and_b32_e32 v201, 0xffff0000, v206
	v_lshlrev_b32_e32 v202, 16, v207
	v_and_b32_e32 v203, 0xffff0000, v207
	v_pk_add_f32 v[180:181], v[180:181], v[196:197] neg_lo:[0,1] neg_hi:[0,1]
	v_pk_add_f32 v[182:183], v[182:183], v[198:199] neg_lo:[0,1] neg_hi:[0,1]
	v_pk_add_f32 v[184:185], v[184:185], v[200:201] neg_lo:[0,1] neg_hi:[0,1]
	v_pk_add_f32 v[186:187], v[186:187], v[202:203] neg_lo:[0,1] neg_hi:[0,1]
	s_add_i32 s2, s5, 2
	v_min_u32_e32 v217, s2, v219
	v_cvt_f32_u32_e32 v217, v217
	v_rcp_f32_e32 v216, v217
	s_waitcnt vmcnt(29)
	v_lshlrev_b32_e32 v188, 16, v64
	v_and_b32_e32 v189, 0xffff0000, v64
	v_lshlrev_b32_e32 v190, 16, v65
	v_and_b32_e32 v191, 0xffff0000, v65
	v_lshlrev_b32_e32 v192, 16, v66
	v_and_b32_e32 v193, 0xffff0000, v66
	v_lshlrev_b32_e32 v194, 16, v67
	v_and_b32_e32 v195, 0xffff0000, v67
	v_pk_add_f32 v[180:181], v[180:181], v[188:189]
	v_pk_add_f32 v[182:183], v[182:183], v[190:191]
	v_pk_add_f32 v[184:185], v[184:185], v[192:193]
	v_pk_add_f32 v[186:187], v[186:187], v[194:195]
	v_pk_fma_f32 v[196:197], v[180:181], v[216:217], v[188:189] op_sel_hi:[1,0,1] neg_lo:[0,0,1] neg_hi:[0,0,1]
	v_pk_fma_f32 v[198:199], v[182:183], v[216:217], v[190:191] op_sel_hi:[1,0,1] neg_lo:[0,0,1] neg_hi:[0,0,1]
	v_pk_fma_f32 v[200:201], v[184:185], v[216:217], v[192:193] op_sel_hi:[1,0,1] neg_lo:[0,0,1] neg_hi:[0,0,1]
	v_pk_fma_f32 v[202:203], v[186:187], v[216:217], v[194:195] op_sel_hi:[1,0,1] neg_lo:[0,0,1] neg_hi:[0,0,1]
	v_cvt_pk_bf16_f32 v212, v196, v197
	v_cvt_pk_bf16_f32 v213, v198, v199
	v_cvt_pk_bf16_f32 v214, v200, v201
	v_cvt_pk_bf16_f32 v215, v202, v203
	s_add_u32 s20, s26, 0x1000
	s_addc_u32 s21, s27, 0
	global_store_dwordx4 v220, v[212:215], s[20:21]
	v_cndmask_b32_e64 v204, v36, v4, s[8:9]
	v_cndmask_b32_e64 v205, v37, v5, s[8:9]
	v_cndmask_b32_e64 v206, v38, v6, s[8:9]
	v_cndmask_b32_e64 v207, v39, v7, s[8:9]
	v_lshlrev_b32_e32 v196, 16, v204
	v_and_b32_e32 v197, 0xffff0000, v204
	v_lshlrev_b32_e32 v198, 16, v205
	v_and_b32_e32 v199, 0xffff0000, v205
	v_lshlrev_b32_e32 v200, 16, v206
	v_and_b32_e32 v201, 0xffff0000, v206
	v_lshlrev_b32_e32 v202, 16, v207
	v_and_b32_e32 v203, 0xffff0000, v207
	v_pk_add_f32 v[180:181], v[180:181], v[196:197] neg_lo:[0,1] neg_hi:[0,1]
	v_pk_add_f32 v[182:183], v[182:183], v[198:199] neg_lo:[0,1] neg_hi:[0,1]
	v_pk_add_f32 v[184:185], v[184:185], v[200:201] neg_lo:[0,1] neg_hi:[0,1]
	v_pk_add_f32 v[186:187], v[186:187], v[202:203] neg_lo:[0,1] neg_hi:[0,1]
	s_add_i32 s2, s5, 3
	v_min_u32_e32 v217, s2, v219
	v_cvt_f32_u32_e32 v217, v217
	v_rcp_f32_e32 v216, v217
	s_waitcnt vmcnt(29)
	v_lshlrev_b32_e32 v188, 16, v68
	v_and_b32_e32 v189, 0xffff0000, v68
	v_lshlrev_b32_e32 v190, 16, v69
	v_and_b32_e32 v191, 0xffff0000, v69
	v_lshlrev_b32_e32 v192, 16, v70
	v_and_b32_e32 v193, 0xffff0000, v70
	v_lshlrev_b32_e32 v194, 16, v71
	v_and_b32_e32 v195, 0xffff0000, v71
	v_pk_add_f32 v[180:181], v[180:181], v[188:189]
	v_pk_add_f32 v[182:183], v[182:183], v[190:191]
	v_pk_add_f32 v[184:185], v[184:185], v[192:193]
	v_pk_add_f32 v[186:187], v[186:187], v[194:195]
	v_pk_fma_f32 v[196:197], v[180:181], v[216:217], v[188:189] op_sel_hi:[1,0,1] neg_lo:[0,0,1] neg_hi:[0,0,1]
	v_pk_fma_f32 v[198:199], v[182:183], v[216:217], v[190:191] op_sel_hi:[1,0,1] neg_lo:[0,0,1] neg_hi:[0,0,1]
	v_pk_fma_f32 v[200:201], v[184:185], v[216:217], v[192:193] op_sel_hi:[1,0,1] neg_lo:[0,0,1] neg_hi:[0,0,1]
	v_pk_fma_f32 v[202:203], v[186:187], v[216:217], v[194:195] op_sel_hi:[1,0,1] neg_lo:[0,0,1] neg_hi:[0,0,1]
	v_cvt_pk_bf16_f32 v208, v196, v197
	v_cvt_pk_bf16_f32 v209, v198, v199
	v_cvt_pk_bf16_f32 v210, v200, v201
	v_cvt_pk_bf16_f32 v211, v202, v203
	s_add_u32 s20, s26, 0x2000
	s_addc_u32 s21, s27, 0
	global_store_dwordx4 v220, v[208:211], s[20:21]
	v_cndmask_b32_e64 v204, v40, v8, s[8:9]
	v_cndmask_b32_e64 v205, v41, v9, s[8:9]
	v_cndmask_b32_e64 v206, v42, v10, s[8:9]
	v_cndmask_b32_e64 v207, v43, v11, s[8:9]
	v_lshlrev_b32_e32 v196, 16, v204
	v_and_b32_e32 v197, 0xffff0000, v204
	v_lshlrev_b32_e32 v198, 16, v205
	v_and_b32_e32 v199, 0xffff0000, v205
	v_lshlrev_b32_e32 v200, 16, v206
	v_and_b32_e32 v201, 0xffff0000, v206
	v_lshlrev_b32_e32 v202, 16, v207
	v_and_b32_e32 v203, 0xffff0000, v207
	v_pk_add_f32 v[180:181], v[180:181], v[196:197] neg_lo:[0,1] neg_hi:[0,1]
	v_pk_add_f32 v[182:183], v[182:183], v[198:199] neg_lo:[0,1] neg_hi:[0,1]
	v_pk_add_f32 v[184:185], v[184:185], v[200:201] neg_lo:[0,1] neg_hi:[0,1]
	v_pk_add_f32 v[186:187], v[186:187], v[202:203] neg_lo:[0,1] neg_hi:[0,1]
	s_add_i32 s2, s5, 4
	v_min_u32_e32 v217, s2, v219
	v_cvt_f32_u32_e32 v217, v217
	v_rcp_f32_e32 v216, v217
	s_waitcnt vmcnt(29)
	v_lshlrev_b32_e32 v188, 16, v72
	v_and_b32_e32 v189, 0xffff0000, v72
	v_lshlrev_b32_e32 v190, 16, v73
	v_and_b32_e32 v191, 0xffff0000, v73
	v_lshlrev_b32_e32 v192, 16, v74
	v_and_b32_e32 v193, 0xffff0000, v74
	v_lshlrev_b32_e32 v194, 16, v75
	v_and_b32_e32 v195, 0xffff0000, v75
	v_pk_add_f32 v[180:181], v[180:181], v[188:189]
	v_pk_add_f32 v[182:183], v[182:183], v[190:191]
	v_pk_add_f32 v[184:185], v[184:185], v[192:193]
	v_pk_add_f32 v[186:187], v[186:187], v[194:195]
	v_pk_fma_f32 v[196:197], v[180:181], v[216:217], v[188:189] op_sel_hi:[1,0,1] neg_lo:[0,0,1] neg_hi:[0,0,1]
	v_pk_fma_f32 v[198:199], v[182:183], v[216:217], v[190:191] op_sel_hi:[1,0,1] neg_lo:[0,0,1] neg_hi:[0,0,1]
	v_pk_fma_f32 v[200:201], v[184:185], v[216:217], v[192:193] op_sel_hi:[1,0,1] neg_lo:[0,0,1] neg_hi:[0,0,1]
	v_pk_fma_f32 v[202:203], v[186:187], v[216:217], v[194:195] op_sel_hi:[1,0,1] neg_lo:[0,0,1] neg_hi:[0,0,1]
	v_cvt_pk_bf16_f32 v212, v196, v197
	v_cvt_pk_bf16_f32 v213, v198, v199
	v_cvt_pk_bf16_f32 v214, v200, v201
	v_cvt_pk_bf16_f32 v215, v202, v203
	s_add_u32 s20, s26, 0x3000
	s_addc_u32 s21, s27, 0
	global_store_dwordx4 v220, v[212:215], s[20:21]
	v_cndmask_b32_e64 v204, v44, v12, s[8:9]
	v_cndmask_b32_e64 v205, v45, v13, s[8:9]
	v_cndmask_b32_e64 v206, v46, v14, s[8:9]
	v_cndmask_b32_e64 v207, v47, v15, s[8:9]
	v_lshlrev_b32_e32 v196, 16, v204
	v_and_b32_e32 v197, 0xffff0000, v204
	v_lshlrev_b32_e32 v198, 16, v205
	v_and_b32_e32 v199, 0xffff0000, v205
	v_lshlrev_b32_e32 v200, 16, v206
	v_and_b32_e32 v201, 0xffff0000, v206
	v_lshlrev_b32_e32 v202, 16, v207
	v_and_b32_e32 v203, 0xffff0000, v207
	v_pk_add_f32 v[180:181], v[180:181], v[196:197] neg_lo:[0,1] neg_hi:[0,1]
	v_pk_add_f32 v[182:183], v[182:183], v[198:199] neg_lo:[0,1] neg_hi:[0,1]
	v_pk_add_f32 v[184:185], v[184:185], v[200:201] neg_lo:[0,1] neg_hi:[0,1]
	v_pk_add_f32 v[186:187], v[186:187], v[202:203] neg_lo:[0,1] neg_hi:[0,1]
	s_add_i32 s2, s5, 5
	v_min_u32_e32 v217, s2, v219
	v_cvt_f32_u32_e32 v217, v217
	v_rcp_f32_e32 v216, v217
	s_waitcnt vmcnt(29)
	v_lshlrev_b32_e32 v188, 16, v76
	v_and_b32_e32 v189, 0xffff0000, v76
	v_lshlrev_b32_e32 v190, 16, v77
	v_and_b32_e32 v191, 0xffff0000, v77
	v_lshlrev_b32_e32 v192, 16, v78
	v_and_b32_e32 v193, 0xffff0000, v78
	v_lshlrev_b32_e32 v194, 16, v79
	v_and_b32_e32 v195, 0xffff0000, v79
	v_pk_add_f32 v[180:181], v[180:181], v[188:189]
	v_pk_add_f32 v[182:183], v[182:183], v[190:191]
	v_pk_add_f32 v[184:185], v[184:185], v[192:193]
	v_pk_add_f32 v[186:187], v[186:187], v[194:195]
	v_pk_fma_f32 v[196:197], v[180:181], v[216:217], v[188:189] op_sel_hi:[1,0,1] neg_lo:[0,0,1] neg_hi:[0,0,1]
	v_pk_fma_f32 v[198:199], v[182:183], v[216:217], v[190:191] op_sel_hi:[1,0,1] neg_lo:[0,0,1] neg_hi:[0,0,1]
	v_pk_fma_f32 v[200:201], v[184:185], v[216:217], v[192:193] op_sel_hi:[1,0,1] neg_lo:[0,0,1] neg_hi:[0,0,1]
	v_pk_fma_f32 v[202:203], v[186:187], v[216:217], v[194:195] op_sel_hi:[1,0,1] neg_lo:[0,0,1] neg_hi:[0,0,1]
	v_cvt_pk_bf16_f32 v208, v196, v197
	v_cvt_pk_bf16_f32 v209, v198, v199
	v_cvt_pk_bf16_f32 v210, v200, v201
	v_cvt_pk_bf16_f32 v211, v202, v203
	s_add_u32 s20, s26, 0x4000
	s_addc_u32 s21, s27, 0
	global_store_dwordx4 v220, v[208:211], s[20:21]
	v_cndmask_b32_e64 v204, v48, v16, s[8:9]
	v_cndmask_b32_e64 v205, v49, v17, s[8:9]
	v_cndmask_b32_e64 v206, v50, v18, s[8:9]
	v_cndmask_b32_e64 v207, v51, v19, s[8:9]
	v_lshlrev_b32_e32 v196, 16, v204
	v_and_b32_e32 v197, 0xffff0000, v204
	v_lshlrev_b32_e32 v198, 16, v205
	v_and_b32_e32 v199, 0xffff0000, v205
	v_lshlrev_b32_e32 v200, 16, v206
	v_and_b32_e32 v201, 0xffff0000, v206
	v_lshlrev_b32_e32 v202, 16, v207
	v_and_b32_e32 v203, 0xffff0000, v207
	v_pk_add_f32 v[180:181], v[180:181], v[196:197] neg_lo:[0,1] neg_hi:[0,1]
	v_pk_add_f32 v[182:183], v[182:183], v[198:199] neg_lo:[0,1] neg_hi:[0,1]
	v_pk_add_f32 v[184:185], v[184:185], v[200:201] neg_lo:[0,1] neg_hi:[0,1]
	v_pk_add_f32 v[186:187], v[186:187], v[202:203] neg_lo:[0,1] neg_hi:[0,1]
	s_add_i32 s2, s5, 6
	v_min_u32_e32 v217, s2, v219
	v_cvt_f32_u32_e32 v217, v217
	v_rcp_f32_e32 v216, v217
	s_waitcnt vmcnt(29)
	v_lshlrev_b32_e32 v188, 16, v80
	v_and_b32_e32 v189, 0xffff0000, v80
	v_lshlrev_b32_e32 v190, 16, v81
	v_and_b32_e32 v191, 0xffff0000, v81
	v_lshlrev_b32_e32 v192, 16, v82
	v_and_b32_e32 v193, 0xffff0000, v82
	v_lshlrev_b32_e32 v194, 16, v83
	v_and_b32_e32 v195, 0xffff0000, v83
	v_pk_add_f32 v[180:181], v[180:181], v[188:189]
	v_pk_add_f32 v[182:183], v[182:183], v[190:191]
	v_pk_add_f32 v[184:185], v[184:185], v[192:193]
	v_pk_add_f32 v[186:187], v[186:187], v[194:195]
	v_pk_fma_f32 v[196:197], v[180:181], v[216:217], v[188:189] op_sel_hi:[1,0,1] neg_lo:[0,0,1] neg_hi:[0,0,1]
	v_pk_fma_f32 v[198:199], v[182:183], v[216:217], v[190:191] op_sel_hi:[1,0,1] neg_lo:[0,0,1] neg_hi:[0,0,1]
	v_pk_fma_f32 v[200:201], v[184:185], v[216:217], v[192:193] op_sel_hi:[1,0,1] neg_lo:[0,0,1] neg_hi:[0,0,1]
	v_pk_fma_f32 v[202:203], v[186:187], v[216:217], v[194:195] op_sel_hi:[1,0,1] neg_lo:[0,0,1] neg_hi:[0,0,1]
	v_cvt_pk_bf16_f32 v212, v196, v197
	v_cvt_pk_bf16_f32 v213, v198, v199
	v_cvt_pk_bf16_f32 v214, v200, v201
	v_cvt_pk_bf16_f32 v215, v202, v203
	s_add_u32 s20, s26, 0x5000
	s_addc_u32 s21, s27, 0
	global_store_dwordx4 v220, v[212:215], s[20:21]
	v_cndmask_b32_e64 v204, v52, v20, s[8:9]
	v_cndmask_b32_e64 v205, v53, v21, s[8:9]
	v_cndmask_b32_e64 v206, v54, v22, s[8:9]
	v_cndmask_b32_e64 v207, v55, v23, s[8:9]
	v_lshlrev_b32_e32 v196, 16, v204
	v_and_b32_e32 v197, 0xffff0000, v204
	v_lshlrev_b32_e32 v198, 16, v205
	v_and_b32_e32 v199, 0xffff0000, v205
	v_lshlrev_b32_e32 v200, 16, v206
	v_and_b32_e32 v201, 0xffff0000, v206
	v_lshlrev_b32_e32 v202, 16, v207
	v_and_b32_e32 v203, 0xffff0000, v207
	v_pk_add_f32 v[180:181], v[180:181], v[196:197] neg_lo:[0,1] neg_hi:[0,1]
	v_pk_add_f32 v[182:183], v[182:183], v[198:199] neg_lo:[0,1] neg_hi:[0,1]
	v_pk_add_f32 v[184:185], v[184:185], v[200:201] neg_lo:[0,1] neg_hi:[0,1]
	v_pk_add_f32 v[186:187], v[186:187], v[202:203] neg_lo:[0,1] neg_hi:[0,1]
	s_add_i32 s2, s5, 7
	v_min_u32_e32 v217, s2, v219
	v_cvt_f32_u32_e32 v217, v217
	v_rcp_f32_e32 v216, v217
	s_waitcnt vmcnt(29)
	v_lshlrev_b32_e32 v188, 16, v84
	v_and_b32_e32 v189, 0xffff0000, v84
	v_lshlrev_b32_e32 v190, 16, v85
	v_and_b32_e32 v191, 0xffff0000, v85
	v_lshlrev_b32_e32 v192, 16, v86
	v_and_b32_e32 v193, 0xffff0000, v86
	v_lshlrev_b32_e32 v194, 16, v87
	v_and_b32_e32 v195, 0xffff0000, v87
	v_pk_add_f32 v[180:181], v[180:181], v[188:189]
	v_pk_add_f32 v[182:183], v[182:183], v[190:191]
	v_pk_add_f32 v[184:185], v[184:185], v[192:193]
	v_pk_add_f32 v[186:187], v[186:187], v[194:195]
	v_pk_fma_f32 v[196:197], v[180:181], v[216:217], v[188:189] op_sel_hi:[1,0,1] neg_lo:[0,0,1] neg_hi:[0,0,1]
	v_pk_fma_f32 v[198:199], v[182:183], v[216:217], v[190:191] op_sel_hi:[1,0,1] neg_lo:[0,0,1] neg_hi:[0,0,1]
	v_pk_fma_f32 v[200:201], v[184:185], v[216:217], v[192:193] op_sel_hi:[1,0,1] neg_lo:[0,0,1] neg_hi:[0,0,1]
	v_pk_fma_f32 v[202:203], v[186:187], v[216:217], v[194:195] op_sel_hi:[1,0,1] neg_lo:[0,0,1] neg_hi:[0,0,1]
	v_cvt_pk_bf16_f32 v208, v196, v197
	v_cvt_pk_bf16_f32 v209, v198, v199
	v_cvt_pk_bf16_f32 v210, v200, v201
	v_cvt_pk_bf16_f32 v211, v202, v203
	s_add_u32 s20, s26, 0x6000
	s_addc_u32 s21, s27, 0
	global_store_dwordx4 v220, v[208:211], s[20:21]
	v_cndmask_b32_e64 v204, v56, v24, s[8:9]
	v_cndmask_b32_e64 v205, v57, v25, s[8:9]
	v_cndmask_b32_e64 v206, v58, v26, s[8:9]
	v_cndmask_b32_e64 v207, v59, v27, s[8:9]
	v_lshlrev_b32_e32 v196, 16, v204
	v_and_b32_e32 v197, 0xffff0000, v204
	v_lshlrev_b32_e32 v198, 16, v205
	v_and_b32_e32 v199, 0xffff0000, v205
	v_lshlrev_b32_e32 v200, 16, v206
	v_and_b32_e32 v201, 0xffff0000, v206
	v_lshlrev_b32_e32 v202, 16, v207
	v_and_b32_e32 v203, 0xffff0000, v207
	v_pk_add_f32 v[180:181], v[180:181], v[196:197] neg_lo:[0,1] neg_hi:[0,1]
	v_pk_add_f32 v[182:183], v[182:183], v[198:199] neg_lo:[0,1] neg_hi:[0,1]
	v_pk_add_f32 v[184:185], v[184:185], v[200:201] neg_lo:[0,1] neg_hi:[0,1]
	v_pk_add_f32 v[186:187], v[186:187], v[202:203] neg_lo:[0,1] neg_hi:[0,1]
	s_add_i32 s2, s5, 8
	v_min_u32_e32 v217, s2, v219
	v_cvt_f32_u32_e32 v217, v217
	v_rcp_f32_e32 v216, v217
	s_waitcnt vmcnt(29)
	v_lshlrev_b32_e32 v188, 16, v88
	v_and_b32_e32 v189, 0xffff0000, v88
	v_lshlrev_b32_e32 v190, 16, v89
	v_and_b32_e32 v191, 0xffff0000, v89
	v_lshlrev_b32_e32 v192, 16, v90
	v_and_b32_e32 v193, 0xffff0000, v90
	v_lshlrev_b32_e32 v194, 16, v91
	v_and_b32_e32 v195, 0xffff0000, v91
	v_pk_add_f32 v[180:181], v[180:181], v[188:189]
	v_pk_add_f32 v[182:183], v[182:183], v[190:191]
	v_pk_add_f32 v[184:185], v[184:185], v[192:193]
	v_pk_add_f32 v[186:187], v[186:187], v[194:195]
	v_pk_fma_f32 v[196:197], v[180:181], v[216:217], v[188:189] op_sel_hi:[1,0,1] neg_lo:[0,0,1] neg_hi:[0,0,1]
	v_pk_fma_f32 v[198:199], v[182:183], v[216:217], v[190:191] op_sel_hi:[1,0,1] neg_lo:[0,0,1] neg_hi:[0,0,1]
	v_pk_fma_f32 v[200:201], v[184:185], v[216:217], v[192:193] op_sel_hi:[1,0,1] neg_lo:[0,0,1] neg_hi:[0,0,1]
	v_pk_fma_f32 v[202:203], v[186:187], v[216:217], v[194:195] op_sel_hi:[1,0,1] neg_lo:[0,0,1] neg_hi:[0,0,1]
	v_cvt_pk_bf16_f32 v212, v196, v197
	v_cvt_pk_bf16_f32 v213, v198, v199
	v_cvt_pk_bf16_f32 v214, v200, v201
	v_cvt_pk_bf16_f32 v215, v202, v203
	s_add_u32 s20, s26, 0x7000
	s_addc_u32 s21, s27, 0
	global_store_dwordx4 v220, v[212:215], s[20:21]
	s_add_u32 s20, s24, 0x8000
	s_addc_u32 s21, s25, 0
	global_load_dwordx4 v[0:3], v221, s[20:21]
	global_load_dwordx4 v[4:7], v221, s[20:21] offset:2048
	s_add_u32 s20, s24, 0xc000
	s_addc_u32 s21, s25, 0
	global_load_dwordx4 v[8:11], v221, s[20:21]
	global_load_dwordx4 v[12:15], v221, s[20:21] offset:2048
	s_add_u32 s20, s24, 0x10000
	s_addc_u32 s21, s25, 0
	global_load_dwordx4 v[16:19], v221, s[20:21]
	global_load_dwordx4 v[20:23], v221, s[20:21] offset:2048
	s_add_u32 s20, s24, 0x14000
	s_addc_u32 s21, s25, 0
	global_load_dwordx4 v[24:27], v221, s[20:21]
	global_load_dwordx4 v[28:31], v221, s[20:21] offset:2048
	s_add_u32 s20, s24, 0x18000
	s_addc_u32 s21, s25, 0
	global_load_dwordx4 v[32:35], v221, s[20:21]
	global_load_dwordx4 v[36:39], v221, s[20:21] offset:2048
	s_add_u32 s20, s24, 0x1c000
	s_addc_u32 s21, s25, 0
	global_load_dwordx4 v[40:43], v221, s[20:21]
	global_load_dwordx4 v[44:47], v221, s[20:21] offset:2048
	s_waitcnt vmcnt(26)
	s_add_i32 s2, s5, -2
	s_cmp_lt_i32 s2, 0
	s_cselect_b32 s2, 0, -1
	v_and_b32_e32 v148, s2, v148
	v_and_b32_e32 v149, s2, v149
	v_and_b32_e32 v150, s2, v150
	v_and_b32_e32 v151, s2, v151
	v_lshlrev_b32_e32 v180, 16, v148
	v_and_b32_e32 v181, 0xffff0000, v148
	v_lshlrev_b32_e32 v182, 16, v149
	v_and_b32_e32 v183, 0xffff0000, v149
	v_lshlrev_b32_e32 v184, 16, v150
	v_and_b32_e32 v185, 0xffff0000, v150
	v_lshlrev_b32_e32 v186, 16, v151
	v_and_b32_e32 v187, 0xffff0000, v151
	v_lshlrev_b32_e32 v188, 16, v152
	v_and_b32_e32 v189, 0xffff0000, v152
	v_lshlrev_b32_e32 v190, 16, v153
	v_and_b32_e32 v191, 0xffff0000, v153
	v_lshlrev_b32_e32 v192, 16, v154
	v_and_b32_e32 v193, 0xffff0000, v154
	v_lshlrev_b32_e32 v194, 16, v155
	v_and_b32_e32 v195, 0xffff0000, v155
	v_pk_mul_f32 v[48:49], v[180:181], v[188:189]
	v_pk_mul_f32 v[50:51], v[182:183], v[190:191]
	v_pk_mul_f32 v[52:53], v[184:185], v[192:193]
	v_pk_mul_f32 v[54:55], v[186:187], v[194:195]
	s_waitcnt vmcnt(24)
	s_add_i32 s2, s5, -1
	s_cmp_lt_i32 s2, 0
	s_cselect_b32 s2, 0, -1
	v_and_b32_e32 v156, s2, v156
	v_and_b32_e32 v157, s2, v157
	v_and_b32_e32 v158, s2, v158
	v_and_b32_e32 v159, s2, v159
	v_lshlrev_b32_e32 v180, 16, v156
	v_and_b32_e32 v181, 0xffff0000, v156
	v_lshlrev_b32_e32 v182, 16, v157
	v_and_b32_e32 v183, 0xffff0000, v157
	v_lshlrev_b32_e32 v184, 16, v158
	v_and_b32_e32 v185, 0xffff0000, v158
	v_lshlrev_b32_e32 v186, 16, v159
	v_and_b32_e32 v187, 0xffff0000, v159
	v_lshlrev_b32_e32 v188, 16, v160
	v_and_b32_e32 v189, 0xffff0000, v160
	v_lshlrev_b32_e32 v190, 16, v161
	v_and_b32_e32 v191, 0xffff0000, v161
	v_lshlrev_b32_e32 v192, 16, v162
	v_and_b32_e32 v193, 0xffff0000, v162
	v_lshlrev_b32_e32 v194, 16, v163
	v_and_b32_e32 v195, 0xffff0000, v163
	v_pk_mul_f32 v[56:57], v[180:181], v[188:189]
	v_pk_mul_f32 v[58:59], v[182:183], v[190:191]
	v_pk_mul_f32 v[60:61], v[184:185], v[192:193]
	v_pk_mul_f32 v[62:63], v[186:187], v[194:195]
	s_waitcnt vmcnt(22)
	v_lshlrev_b32_e32 v180, 16, v164
	v_and_b32_e32 v181, 0xffff0000, v164
	v_lshlrev_b32_e32 v182, 16, v165
	v_and_b32_e32 v183, 0xffff0000, v165
	v_lshlrev_b32_e32 v184, 16, v166
	v_and_b32_e32 v185, 0xffff0000, v166
	v_lshlrev_b32_e32 v186, 16, v167
	v_and_b32_e32 v187, 0xffff0000, v167
	v_lshlrev_b32_e32 v188, 16, v168
	v_and_b32_e32 v189, 0xffff0000, v168
	v_lshlrev_b32_e32 v190, 16, v169
	v_and_b32_e32 v191, 0xffff0000, v169
	v_lshlrev_b32_e32 v192, 16, v170
	v_and_b32_e32 v193, 0xffff0000, v170
	v_lshlrev_b32_e32 v194, 16, v171
	v_and_b32_e32 v195, 0xffff0000, v171
	v_pk_mul_f32 v[64:65], v[180:181], v[188:189]
	v_pk_mul_f32 v[66:67], v[182:183], v[190:191]
	v_pk_mul_f32 v[68:69], v[184:185], v[192:193]
	v_pk_mul_f32 v[70:71], v[186:187], v[194:195]
	v_pk_mul_f32 v[72:73], v[92:93], v[48:49]
	v_pk_mul_f32 v[74:75], v[94:95], v[50:51]
	v_pk_mul_f32 v[76:77], v[96:97], v[52:53]
	v_pk_mul_f32 v[78:79], v[98:99], v[54:55]
	v_pk_fma_f32 v[72:73], v[100:101], v[56:57], v[72:73]
	v_pk_fma_f32 v[74:75], v[102:103], v[58:59], v[74:75]
	v_pk_fma_f32 v[76:77], v[104:105], v[60:61], v[76:77]
	v_pk_fma_f32 v[78:79], v[106:107], v[62:63], v[78:79]
	v_pk_fma_f32 v[72:73], v[108:109], v[64:65], v[72:73]
	v_pk_fma_f32 v[74:75], v[110:111], v[66:67], v[74:75]
	v_pk_fma_f32 v[76:77], v[112:113], v[68:69], v[76:77]
	v_pk_fma_f32 v[78:79], v[114:115], v[70:71], v[78:79]
	s_waitcnt vmcnt(35)
	v_lshlrev_b32_e32 v196, 16, v116
	v_and_b32_e32 v197, 0xffff0000, v116
	v_lshlrev_b32_e32 v198, 16, v117
	v_and_b32_e32 v199, 0xffff0000, v117
	v_lshlrev_b32_e32 v200, 16, v118
	v_and_b32_e32 v201, 0xffff0000, v118
	v_lshlrev_b32_e32 v202, 16, v119
	v_and_b32_e32 v203, 0xffff0000, v119
	v_pk_mul_f32 v[72:73], v[72:73], v[196:197]
	v_pk_mul_f32 v[74:75], v[74:75], v[198:199]
	v_pk_mul_f32 v[76:77], v[76:77], v[200:201]
	v_pk_mul_f32 v[78:79], v[78:79], v[202:203]
	v_cvt_pk_bf16_f32 v208, v72, v73
	v_cvt_pk_bf16_f32 v209, v74, v75
	v_cvt_pk_bf16_f32 v210, v76, v77
	v_cvt_pk_bf16_f32 v211, v78, v79
	global_store_dwordx4 v220, v[208:211], s[26:27] offset:2048
	s_waitcnt vmcnt(21)
	v_lshlrev_b32_e32 v180, 16, v172
	v_and_b32_e32 v181, 0xffff0000, v172
	v_lshlrev_b32_e32 v182, 16, v173
	v_and_b32_e32 v183, 0xffff0000, v173
	v_lshlrev_b32_e32 v184, 16, v174
	v_and_b32_e32 v185, 0xffff0000, v174
	v_lshlrev_b32_e32 v186, 16, v175
	v_and_b32_e32 v187, 0xffff0000, v175
	v_lshlrev_b32_e32 v188, 16, v176
	v_and_b32_e32 v189, 0xffff0000, v176
	v_lshlrev_b32_e32 v190, 16, v177
	v_and_b32_e32 v191, 0xffff0000, v177
	v_lshlrev_b32_e32 v192, 16, v178
	v_and_b32_e32 v193, 0xffff0000, v178
	v_lshlrev_b32_e32 v194, 16, v179
	v_and_b32_e32 v195, 0xffff0000, v179
	v_pk_mul_f32 v[48:49], v[180:181], v[188:189]
	v_pk_mul_f32 v[50:51], v[182:183], v[190:191]
	v_pk_mul_f32 v[52:53], v[184:185], v[192:193]
	v_pk_mul_f32 v[54:55], v[186:187], v[194:195]
	v_pk_mul_f32 v[72:73], v[92:93], v[56:57]
	v_pk_mul_f32 v[74:75], v[94:95], v[58:59]
	v_pk_mul_f32 v[76:77], v[96:97], v[60:61]
	v_pk_mul_f32 v[78:79], v[98:99], v[62:63]
	v_pk_fma_f32 v[72:73], v[100:101], v[64:65], v[72:73]
	v_pk_fma_f32 v[74:75], v[102:103], v[66:67], v[74:75]
	v_pk_fma_f32 v[76:77], v[104:105], v[68:69], v[76:77]
	v_pk_fma_f32 v[78:79], v[106:107], v[70:71], v[78:79]
	v_pk_fma_f32 v[72:73], v[108:109], v[48:49], v[72:73]
	v_pk_fma_f32 v[74:75], v[110:111], v[50:51], v[74:75]
	v_pk_fma_f32 v[76:77], v[112:113], v[52:53], v[76:77]
	v_pk_fma_f32 v[78:79], v[114:115], v[54:55], v[78:79]
	s_waitcnt vmcnt(35)
	v_lshlrev_b32_e32 v196, 16, v120
	v_and_b32_e32 v197, 0xffff0000, v120
	v_lshlrev_b32_e32 v198, 16, v121
	v_and_b32_e32 v199, 0xffff0000, v121
	v_lshlrev_b32_e32 v200, 16, v122
	v_and_b32_e32 v201, 0xffff0000, v122
	v_lshlrev_b32_e32 v202, 16, v123
	v_and_b32_e32 v203, 0xffff0000, v123
	v_pk_mul_f32 v[72:73], v[72:73], v[196:197]
	v_pk_mul_f32 v[74:75], v[74:75], v[198:199]
	v_pk_mul_f32 v[76:77], v[76:77], v[200:201]
	v_pk_mul_f32 v[78:79], v[78:79], v[202:203]
	v_cvt_pk_bf16_f32 v212, v72, v73
	v_cvt_pk_bf16_f32 v213, v74, v75
	v_cvt_pk_bf16_f32 v214, v76, v77
	v_cvt_pk_bf16_f32 v215, v78, v79
	s_add_u32 s20, s26, 0x1000
	s_addc_u32 s21, s27, 0
	global_store_dwordx4 v220, v[212:215], s[20:21] offset:2048
	s_waitcnt vmcnt(12)
	v_lshlrev_b32_e32 v180, 16, v0
	v_and_b32_e32 v181, 0xffff0000, v0
	v_lshlrev_b32_e32 v182, 16, v1
	v_and_b32_e32 v183, 0xffff0000, v1
	v_lshlrev_b32_e32 v184, 16, v2
	v_and_b32_e32 v185, 0xffff0000, v2
	v_lshlrev_b32_e32 v186, 16, v3
	v_and_b32_e32 v187, 0xffff0000, v3
	v_lshlrev_b32_e32 v188, 16, v4
	v_and_b32_e32 v189, 0xffff0000, v4
	v_lshlrev_b32_e32 v190, 16, v5
	v_and_b32_e32 v191, 0xffff0000, v5
	v_lshlrev_b32_e32 v192, 16, v6
	v_and_b32_e32 v193, 0xffff0000, v6
	v_lshlrev_b32_e32 v194, 16, v7
	v_and_b32_e32 v195, 0xffff0000, v7
	v_pk_mul_f32 v[56:57], v[180:181], v[188:189]
	v_pk_mul_f32 v[58:59], v[182:183], v[190:191]
	v_pk_mul_f32 v[60:61], v[184:185], v[192:193]
	v_pk_mul_f32 v[62:63], v[186:187], v[194:195]
	v_pk_mul_f32 v[72:73], v[92:93], v[64:65]
	v_pk_mul_f32 v[74:75], v[94:95], v[66:67]
	v_pk_mul_f32 v[76:77], v[96:97], v[68:69]
	v_pk_mul_f32 v[78:79], v[98:99], v[70:71]
	v_pk_fma_f32 v[72:73], v[100:101], v[48:49], v[72:73]
	v_pk_fma_f32 v[74:75], v[102:103], v[50:51], v[74:75]
	v_pk_fma_f32 v[76:77], v[104:105], v[52:53], v[76:77]
	v_pk_fma_f32 v[78:79], v[106:107], v[54:55], v[78:79]
	v_pk_fma_f32 v[72:73], v[108:109], v[56:57], v[72:73]
	v_pk_fma_f32 v[74:75], v[110:111], v[58:59], v[74:75]
	v_pk_fma_f32 v[76:77], v[112:113], v[60:61], v[76:77]
	v_pk_fma_f32 v[78:79], v[114:115], v[62:63], v[78:79]
	s_waitcnt vmcnt(35)
	v_lshlrev_b32_e32 v196, 16, v124
	v_and_b32_e32 v197, 0xffff0000, v124
	v_lshlrev_b32_e32 v198, 16, v125
	v_and_b32_e32 v199, 0xffff0000, v125
	v_lshlrev_b32_e32 v200, 16, v126
	v_and_b32_e32 v201, 0xffff0000, v126
	v_lshlrev_b32_e32 v202, 16, v127
	v_and_b32_e32 v203, 0xffff0000, v127
	v_pk_mul_f32 v[72:73], v[72:73], v[196:197]
	v_pk_mul_f32 v[74:75], v[74:75], v[198:199]
	v_pk_mul_f32 v[76:77], v[76:77], v[200:201]
	v_pk_mul_f32 v[78:79], v[78:79], v[202:203]
	v_cvt_pk_bf16_f32 v208, v72, v73
	v_cvt_pk_bf16_f32 v209, v74, v75
	v_cvt_pk_bf16_f32 v210, v76, v77
	v_cvt_pk_bf16_f32 v211, v78, v79
	s_add_u32 s20, s26, 0x2000
	s_addc_u32 s21, s27, 0
	global_store_dwordx4 v220, v[208:211], s[20:21] offset:2048
	s_waitcnt vmcnt(11)
	v_lshlrev_b32_e32 v180, 16, v8
	v_and_b32_e32 v181, 0xffff0000, v8
	v_lshlrev_b32_e32 v182, 16, v9
	v_and_b32_e32 v183, 0xffff0000, v9
	v_lshlrev_b32_e32 v184, 16, v10
	v_and_b32_e32 v185, 0xffff0000, v10
	v_lshlrev_b32_e32 v186, 16, v11
	v_and_b32_e32 v187, 0xffff0000, v11
	v_lshlrev_b32_e32 v188, 16, v12
	v_and_b32_e32 v189, 0xffff0000, v12
	v_lshlrev_b32_e32 v190, 16, v13
	v_and_b32_e32 v191, 0xffff0000, v13
	v_lshlrev_b32_e32 v192, 16, v14
	v_and_b32_e32 v193, 0xffff0000, v14
	v_lshlrev_b32_e32 v194, 16, v15
	v_and_b32_e32 v195, 0xffff0000, v15
	v_pk_mul_f32 v[64:65], v[180:181], v[188:189]
	v_pk_mul_f32 v[66:67], v[182:183], v[190:191]
	v_pk_mul_f32 v[68:69], v[184:185], v[192:193]
	v_pk_mul_f32 v[70:71], v[186:187], v[194:195]
	v_pk_mul_f32 v[72:73], v[92:93], v[48:49]
	v_pk_mul_f32 v[74:75], v[94:95], v[50:51]
	v_pk_mul_f32 v[76:77], v[96:97], v[52:53]
	v_pk_mul_f32 v[78:79], v[98:99], v[54:55]
	v_pk_fma_f32 v[72:73], v[100:101], v[56:57], v[72:73]
	v_pk_fma_f32 v[74:75], v[102:103], v[58:59], v[74:75]
	v_pk_fma_f32 v[76:77], v[104:105], v[60:61], v[76:77]
	v_pk_fma_f32 v[78:79], v[106:107], v[62:63], v[78:79]
	v_pk_fma_f32 v[72:73], v[108:109], v[64:65], v[72:73]
	v_pk_fma_f32 v[74:75], v[110:111], v[66:67], v[74:75]
	v_pk_fma_f32 v[76:77], v[112:113], v[68:69], v[76:77]
	v_pk_fma_f32 v[78:79], v[114:115], v[70:71], v[78:79]
	s_waitcnt vmcnt(35)
	v_lshlrev_b32_e32 v196, 16, v128
	v_and_b32_e32 v197, 0xffff0000, v128
	v_lshlrev_b32_e32 v198, 16, v129
	v_and_b32_e32 v199, 0xffff0000, v129
	v_lshlrev_b32_e32 v200, 16, v130
	v_and_b32_e32 v201, 0xffff0000, v130
	v_lshlrev_b32_e32 v202, 16, v131
	v_and_b32_e32 v203, 0xffff0000, v131
	v_pk_mul_f32 v[72:73], v[72:73], v[196:197]
	v_pk_mul_f32 v[74:75], v[74:75], v[198:199]
	v_pk_mul_f32 v[76:77], v[76:77], v[200:201]
	v_pk_mul_f32 v[78:79], v[78:79], v[202:203]
	v_cvt_pk_bf16_f32 v212, v72, v73
	v_cvt_pk_bf16_f32 v213, v74, v75
	v_cvt_pk_bf16_f32 v214, v76, v77
	v_cvt_pk_bf16_f32 v215, v78, v79
	s_add_u32 s20, s26, 0x3000
	s_addc_u32 s21, s27, 0
	global_store_dwordx4 v220, v[212:215], s[20:21] offset:2048
	s_waitcnt vmcnt(10)
	v_lshlrev_b32_e32 v180, 16, v16
	v_and_b32_e32 v181, 0xffff0000, v16
	v_lshlrev_b32_e32 v182, 16, v17
	v_and_b32_e32 v183, 0xffff0000, v17
	v_lshlrev_b32_e32 v184, 16, v18
	v_and_b32_e32 v185, 0xffff0000, v18
	v_lshlrev_b32_e32 v186, 16, v19
	v_and_b32_e32 v187, 0xffff0000, v19
	v_lshlrev_b32_e32 v188, 16, v20
	v_and_b32_e32 v189, 0xffff0000, v20
	v_lshlrev_b32_e32 v190, 16, v21
	v_and_b32_e32 v191, 0xffff0000, v21
	v_lshlrev_b32_e32 v192, 16, v22
	v_and_b32_e32 v193, 0xffff0000, v22
	v_lshlrev_b32_e32 v194, 16, v23
	v_and_b32_e32 v195, 0xffff0000, v23
	v_pk_mul_f32 v[48:49], v[180:181], v[188:189]
	v_pk_mul_f32 v[50:51], v[182:183], v[190:191]
	v_pk_mul_f32 v[52:53], v[184:185], v[192:193]
	v_pk_mul_f32 v[54:55], v[186:187], v[194:195]
	v_pk_mul_f32 v[72:73], v[92:93], v[56:57]
	v_pk_mul_f32 v[74:75], v[94:95], v[58:59]
	v_pk_mul_f32 v[76:77], v[96:97], v[60:61]
	v_pk_mul_f32 v[78:79], v[98:99], v[62:63]
	v_pk_fma_f32 v[72:73], v[100:101], v[64:65], v[72:73]
	v_pk_fma_f32 v[74:75], v[102:103], v[66:67], v[74:75]
	v_pk_fma_f32 v[76:77], v[104:105], v[68:69], v[76:77]
	v_pk_fma_f32 v[78:79], v[106:107], v[70:71], v[78:79]
	v_pk_fma_f32 v[72:73], v[108:109], v[48:49], v[72:73]
	v_pk_fma_f32 v[74:75], v[110:111], v[50:51], v[74:75]
	v_pk_fma_f32 v[76:77], v[112:113], v[52:53], v[76:77]
	v_pk_fma_f32 v[78:79], v[114:115], v[54:55], v[78:79]
	s_waitcnt vmcnt(35)
	v_lshlrev_b32_e32 v196, 16, v132
	v_and_b32_e32 v197, 0xffff0000, v132
	v_lshlrev_b32_e32 v198, 16, v133
	v_and_b32_e32 v199, 0xffff0000, v133
	v_lshlrev_b32_e32 v200, 16, v134
	v_and_b32_e32 v201, 0xffff0000, v134
	v_lshlrev_b32_e32 v202, 16, v135
	v_and_b32_e32 v203, 0xffff0000, v135
	v_pk_mul_f32 v[72:73], v[72:73], v[196:197]
	v_pk_mul_f32 v[74:75], v[74:75], v[198:199]
	v_pk_mul_f32 v[76:77], v[76:77], v[200:201]
	v_pk_mul_f32 v[78:79], v[78:79], v[202:203]
	v_cvt_pk_bf16_f32 v208, v72, v73
	v_cvt_pk_bf16_f32 v209, v74, v75
	v_cvt_pk_bf16_f32 v210, v76, v77
	v_cvt_pk_bf16_f32 v211, v78, v79
	s_add_u32 s20, s26, 0x4000
	s_addc_u32 s21, s27, 0
	global_store_dwordx4 v220, v[208:211], s[20:21] offset:2048
	s_waitcnt vmcnt(9)
	v_lshlrev_b32_e32 v180, 16, v24
	v_and_b32_e32 v181, 0xffff0000, v24
	v_lshlrev_b32_e32 v182, 16, v25
	v_and_b32_e32 v183, 0xffff0000, v25
	v_lshlrev_b32_e32 v184, 16, v26
	v_and_b32_e32 v185, 0xffff0000, v26
	v_lshlrev_b32_e32 v186, 16, v27
	v_and_b32_e32 v187, 0xffff0000, v27
	v_lshlrev_b32_e32 v188, 16, v28
	v_and_b32_e32 v189, 0xffff0000, v28
	v_lshlrev_b32_e32 v190, 16, v29
	v_and_b32_e32 v191, 0xffff0000, v29
	v_lshlrev_b32_e32 v192, 16, v30
	v_and_b32_e32 v193, 0xffff0000, v30
	v_lshlrev_b32_e32 v194, 16, v31
	v_and_b32_e32 v195, 0xffff0000, v31
	v_pk_mul_f32 v[56:57], v[180:181], v[188:189]
	v_pk_mul_f32 v[58:59], v[182:183], v[190:191]
	v_pk_mul_f32 v[60:61], v[184:185], v[192:193]
	v_pk_mul_f32 v[62:63], v[186:187], v[194:195]
	v_pk_mul_f32 v[72:73], v[92:93], v[64:65]
	v_pk_mul_f32 v[74:75], v[94:95], v[66:67]
	v_pk_mul_f32 v[76:77], v[96:97], v[68:69]
	v_pk_mul_f32 v[78:79], v[98:99], v[70:71]
	v_pk_fma_f32 v[72:73], v[100:101], v[48:49], v[72:73]
	v_pk_fma_f32 v[74:75], v[102:103], v[50:51], v[74:75]
	v_pk_fma_f32 v[76:77], v[104:105], v[52:53], v[76:77]
	v_pk_fma_f32 v[78:79], v[106:107], v[54:55], v[78:79]
	v_pk_fma_f32 v[72:73], v[108:109], v[56:57], v[72:73]
	v_pk_fma_f32 v[74:75], v[110:111], v[58:59], v[74:75]
	v_pk_fma_f32 v[76:77], v[112:113], v[60:61], v[76:77]
	v_pk_fma_f32 v[78:79], v[114:115], v[62:63], v[78:79]
	s_waitcnt vmcnt(35)
	v_lshlrev_b32_e32 v196, 16, v136
	v_and_b32_e32 v197, 0xffff0000, v136
	v_lshlrev_b32_e32 v198, 16, v137
	v_and_b32_e32 v199, 0xffff0000, v137
	v_lshlrev_b32_e32 v200, 16, v138
	v_and_b32_e32 v201, 0xffff0000, v138
	v_lshlrev_b32_e32 v202, 16, v139
	v_and_b32_e32 v203, 0xffff0000, v139
	v_pk_mul_f32 v[72:73], v[72:73], v[196:197]
	v_pk_mul_f32 v[74:75], v[74:75], v[198:199]
	v_pk_mul_f32 v[76:77], v[76:77], v[200:201]
	v_pk_mul_f32 v[78:79], v[78:79], v[202:203]
	v_cvt_pk_bf16_f32 v212, v72, v73
	v_cvt_pk_bf16_f32 v213, v74, v75
	v_cvt_pk_bf16_f32 v214, v76, v77
	v_cvt_pk_bf16_f32 v215, v78, v79
	s_add_u32 s20, s26, 0x5000
	s_addc_u32 s21, s27, 0
	global_store_dwordx4 v220, v[212:215], s[20:21] offset:2048
	s_waitcnt vmcnt(8)
	v_lshlrev_b32_e32 v180, 16, v32
	v_and_b32_e32 v181, 0xffff0000, v32
	v_lshlrev_b32_e32 v182, 16, v33
	v_and_b32_e32 v183, 0xffff0000, v33
	v_lshlrev_b32_e32 v184, 16, v34
	v_and_b32_e32 v185, 0xffff0000, v34
	v_lshlrev_b32_e32 v186, 16, v35
	v_and_b32_e32 v187, 0xffff0000, v35
	v_lshlrev_b32_e32 v188, 16, v36
	v_and_b32_e32 v189, 0xffff0000, v36
	v_lshlrev_b32_e32 v190, 16, v37
	v_and_b32_e32 v191, 0xffff0000, v37
	v_lshlrev_b32_e32 v192, 16, v38
	v_and_b32_e32 v193, 0xffff0000, v38
	v_lshlrev_b32_e32 v194, 16, v39
	v_and_b32_e32 v195, 0xffff0000, v39
	v_pk_mul_f32 v[64:65], v[180:181], v[188:189]
	v_pk_mul_f32 v[66:67], v[182:183], v[190:191]
	v_pk_mul_f32 v[68:69], v[184:185], v[192:193]
	v_pk_mul_f32 v[70:71], v[186:187], v[194:195]
	v_pk_mul_f32 v[72:73], v[92:93], v[48:49]
	v_pk_mul_f32 v[74:75], v[94:95], v[50:51]
	v_pk_mul_f32 v[76:77], v[96:97], v[52:53]
	v_pk_mul_f32 v[78:79], v[98:99], v[54:55]
	v_pk_fma_f32 v[72:73], v[100:101], v[56:57], v[72:73]
	v_pk_fma_f32 v[74:75], v[102:103], v[58:59], v[74:75]
	v_pk_fma_f32 v[76:77], v[104:105], v[60:61], v[76:77]
	v_pk_fma_f32 v[78:79], v[106:107], v[62:63], v[78:79]
	v_pk_fma_f32 v[72:73], v[108:109], v[64:65], v[72:73]
	v_pk_fma_f32 v[74:75], v[110:111], v[66:67], v[74:75]
	v_pk_fma_f32 v[76:77], v[112:113], v[68:69], v[76:77]
	v_pk_fma_f32 v[78:79], v[114:115], v[70:71], v[78:79]
	s_waitcnt vmcnt(35)
	v_lshlrev_b32_e32 v196, 16, v140
	v_and_b32_e32 v197, 0xffff0000, v140
	v_lshlrev_b32_e32 v198, 16, v141
	v_and_b32_e32 v199, 0xffff0000, v141
	v_lshlrev_b32_e32 v200, 16, v142
	v_and_b32_e32 v201, 0xffff0000, v142
	v_lshlrev_b32_e32 v202, 16, v143
	v_and_b32_e32 v203, 0xffff0000, v143
	v_pk_mul_f32 v[72:73], v[72:73], v[196:197]
	v_pk_mul_f32 v[74:75], v[74:75], v[198:199]
	v_pk_mul_f32 v[76:77], v[76:77], v[200:201]
	v_pk_mul_f32 v[78:79], v[78:79], v[202:203]
	v_cvt_pk_bf16_f32 v208, v72, v73
	v_cvt_pk_bf16_f32 v209, v74, v75
	v_cvt_pk_bf16_f32 v210, v76, v77
	v_cvt_pk_bf16_f32 v211, v78, v79
	s_add_u32 s20, s26, 0x6000
	s_addc_u32 s21, s27, 0
	global_store_dwordx4 v220, v[208:211], s[20:21] offset:2048
	s_waitcnt vmcnt(7)
	v_lshlrev_b32_e32 v180, 16, v40
	v_and_b32_e32 v181, 0xffff0000, v40
	v_lshlrev_b32_e32 v182, 16, v41
	v_and_b32_e32 v183, 0xffff0000, v41
	v_lshlrev_b32_e32 v184, 16, v42
	v_and_b32_e32 v185, 0xffff0000, v42
	v_lshlrev_b32_e32 v186, 16, v43
	v_and_b32_e32 v187, 0xffff0000, v43
	v_lshlrev_b32_e32 v188, 16, v44
	v_and_b32_e32 v189, 0xffff0000, v44
	v_lshlrev_b32_e32 v190, 16, v45
	v_and_b32_e32 v191, 0xffff0000, v45
	v_lshlrev_b32_e32 v192, 16, v46
	v_and_b32_e32 v193, 0xffff0000, v46
	v_lshlrev_b32_e32 v194, 16, v47
	v_and_b32_e32 v195, 0xffff0000, v47
	v_pk_mul_f32 v[48:49], v[180:181], v[188:189]
	v_pk_mul_f32 v[50:51], v[182:183], v[190:191]
	v_pk_mul_f32 v[52:53], v[184:185], v[192:193]
	v_pk_mul_f32 v[54:55], v[186:187], v[194:195]
	v_pk_mul_f32 v[72:73], v[92:93], v[56:57]
	v_pk_mul_f32 v[74:75], v[94:95], v[58:59]
	v_pk_mul_f32 v[76:77], v[96:97], v[60:61]
	v_pk_mul_f32 v[78:79], v[98:99], v[62:63]
	v_pk_fma_f32 v[72:73], v[100:101], v[64:65], v[72:73]
	v_pk_fma_f32 v[74:75], v[102:103], v[66:67], v[74:75]
	v_pk_fma_f32 v[76:77], v[104:105], v[68:69], v[76:77]
	v_pk_fma_f32 v[78:79], v[106:107], v[70:71], v[78:79]
	v_pk_fma_f32 v[72:73], v[108:109], v[48:49], v[72:73]
	v_pk_fma_f32 v[74:75], v[110:111], v[50:51], v[74:75]
	v_pk_fma_f32 v[76:77], v[112:113], v[52:53], v[76:77]
	v_pk_fma_f32 v[78:79], v[114:115], v[54:55], v[78:79]
	s_waitcnt vmcnt(35)
	v_lshlrev_b32_e32 v196, 16, v144
	v_and_b32_e32 v197, 0xffff0000, v144
	v_lshlrev_b32_e32 v198, 16, v145
	v_and_b32_e32 v199, 0xffff0000, v145
	v_lshlrev_b32_e32 v200, 16, v146
	v_and_b32_e32 v201, 0xffff0000, v146
	v_lshlrev_b32_e32 v202, 16, v147
	v_and_b32_e32 v203, 0xffff0000, v147
	v_pk_mul_f32 v[72:73], v[72:73], v[196:197]
	v_pk_mul_f32 v[74:75], v[74:75], v[198:199]
	v_pk_mul_f32 v[76:77], v[76:77], v[200:201]
	v_pk_mul_f32 v[78:79], v[78:79], v[202:203]
	v_cvt_pk_bf16_f32 v212, v72, v73
	v_cvt_pk_bf16_f32 v213, v74, v75
	v_cvt_pk_bf16_f32 v214, v76, v77
	v_cvt_pk_bf16_f32 v215, v78, v79
	s_add_u32 s20, s26, 0x7000
	s_addc_u32 s21, s27, 0
	global_store_dwordx4 v220, v[212:215], s[20:21] offset:2048
	s_branch .LBB0_387
.Lp2_even:
	s_add_i32 s2, s5, -3
	s_max_i32 s2, s2, 0
	s_lshl_b32 s2, s2, 14
	s_add_u32 s20, s22, s2
	s_addc_u32 s21, s23, 0
	global_load_dwordx4 v[0:3], v220, s[20:21]
	s_add_i32 s2, s5, -2
	s_max_i32 s2, s2, 0
	s_lshl_b32 s2, s2, 14
	s_add_u32 s20, s22, s2
	s_addc_u32 s21, s23, 0
	global_load_dwordx4 v[4:7], v220, s[20:21]
	s_add_i32 s2, s5, -1
	s_max_i32 s2, s2, 0
	s_lshl_b32 s2, s2, 14
	s_add_u32 s20, s22, s2
	s_addc_u32 s21, s23, 0
	global_load_dwordx4 v[8:11], v220, s[20:21]
	global_load_dwordx4 v[12:15], v220, s[24:25]
	s_add_u32 s20, s24, 0x4000
	s_addc_u32 s21, s25, 0
	global_load_dwordx4 v[16:19], v220, s[20:21]
	s_add_u32 s20, s24, 0x8000
	s_addc_u32 s21, s25, 0
	global_load_dwordx4 v[20:23], v220, s[20:21]
	s_add_u32 s20, s24, 0xc000
	s_addc_u32 s21, s25, 0
	global_load_dwordx4 v[24:27], v220, s[20:21]
	s_add_u32 s20, s24, 0x10000
	s_addc_u32 s21, s25, 0
	global_load_dwordx4 v[28:31], v220, s[20:21]
	s_add_u32 s20, s24, 0x14000
	s_addc_u32 s21, s25, 0
	global_load_dwordx4 v[32:35], v220, s[20:21]
	s_add_u32 s20, s24, 0x18000
	s_addc_u32 s21, s25, 0
	global_load_dwordx4 v[36:39], v220, s[20:21]
	s_add_u32 s20, s24, 0x1c000
	s_addc_u32 s21, s25, 0
	global_load_dwordx4 v[40:43], v220, s[20:21]
	global_load_dwordx4 v[92:95], v217, s[82:83]
	global_load_dwordx4 v[96:99], v217, s[82:83] offset:16
	s_add_u32 s20, s82, 0x1000
	s_addc_u32 s21, s83, 0
	global_load_dwordx4 v[100:103], v217, s[20:21]
	global_load_dwordx4 v[104:107], v217, s[20:21] offset:16
	s_add_u32 s20, s82, 0x2000
	s_addc_u32 s21, s83, 0
	global_load_dwordx4 v[108:111], v217, s[20:21]
	global_load_dwordx4 v[112:115], v217, s[20:21] offset:16
	global_load_dwordx4 v[116:119], v220, s[24:25] offset:2048
	s_add_u32 s20, s24, 0x4000
	s_addc_u32 s21, s25, 0
	global_load_dwordx4 v[120:123], v220, s[20:21] offset:2048
	s_add_u32 s20, s24, 0x8000
	s_addc_u32 s21, s25, 0
	global_load_dwordx4 v[124:127], v220, s[20:21] offset:2048
	s_add_u32 s20, s24, 0xc000
	s_addc_u32 s21, s25, 0
	global_load_dwordx4 v[128:131], v220, s[20:21] offset:2048
	s_add_u32 s20, s24, 0x10000
	s_addc_u32 s21, s25, 0
	global_load_dwordx4 v[132:135], v220, s[20:21] offset:2048
	s_add_u32 s20, s24, 0x14000
	s_addc_u32 s21, s25, 0
	global_load_dwordx4 v[136:139], v220, s[20:21] offset:2048
	s_add_u32 s20, s24, 0x18000
	s_addc_u32 s21, s25, 0
	global_load_dwordx4 v[140:143], v220, s[20:21] offset:2048
	s_add_u32 s20, s24, 0x1c000
	s_addc_u32 s21, s25, 0
	global_load_dwordx4 v[144:147], v220, s[20:21] offset:2048
	s_add_i32 s2, s5, -2
	s_max_i32 s2, s2, 0
	s_lshl_b32 s2, s2, 14
	s_add_u32 s20, s22, s2
	s_addc_u32 s21, s23, 0
	global_load_dwordx4 v[148:151], v221, s[20:21]
	global_load_dwordx4 v[152:155], v221, s[20:21] offset:2048
	s_add_i32 s2, s5, -1
	s_max_i32 s2, s2, 0
	s_lshl_b32 s2, s2, 14
	s_add_u32 s20, s22, s2
	s_addc_u32 s21, s23, 0
	global_load_dwordx4 v[156:159], v221, s[20:21]
	global_load_dwordx4 v[160:163], v221, s[20:21] offset:2048
	global_load_dwordx4 v[164:167], v221, s[24:25]
	global_load_dwordx4 v[168:171], v221, s[24:25] offset:2048
	s_add_u32 s20, s24, 0x4000
	s_addc_u32 s21, s25, 0
	global_load_dwordx4 v[172:175], v221, s[20:21]
	global_load_dwordx4 v[176:179], v221, s[20:21] offset:2048
	s_add_u32 s20, s24, 0x8000
	s_addc_u32 s21, s25, 0
	global_load_dwordx4 v[44:47], v221, s[20:21]
	global_load_dwordx4 v[48:51], v221, s[20:21] offset:2048
	s_add_u32 s20, s24, 0xc000
	s_addc_u32 s21, s25, 0
	global_load_dwordx4 v[52:55], v221, s[20:21]
	global_load_dwordx4 v[56:59], v221, s[20:21] offset:2048
	s_add_u32 s20, s24, 0x10000
	s_addc_u32 s21, s25, 0
	global_load_dwordx4 v[60:63], v221, s[20:21]
	global_load_dwordx4 v[64:67], v221, s[20:21] offset:2048
	s_add_u32 s20, s24, 0x14000
	s_addc_u32 s21, s25, 0
	global_load_dwordx4 v[68:71], v221, s[20:21]
	global_load_dwordx4 v[72:75], v221, s[20:21] offset:2048
	s_add_u32 s20, s24, 0x18000
	s_addc_u32 s21, s25, 0
	global_load_dwordx4 v[76:79], v221, s[20:21]
	global_load_dwordx4 v[80:83], v221, s[20:21] offset:2048
	s_add_u32 s20, s24, 0x1c000
	s_addc_u32 s21, s25, 0
	global_load_dwordx4 v[84:87], v221, s[20:21]
	global_load_dwordx4 v[88:91], v221, s[20:21] offset:2048
	v_cndmask_b32_e64 v219, 2, 4, s[8:9]
	v_cndmask_b32_e64 v218, 0, 1.0, s[8:9]
	s_cmp_ge_u32 s5, 3
	s_cbranch_scc1 .Lp2_nomask_even
	s_waitcnt vmcnt(42)
	s_add_i32 s2, s5, -3
	s_cmp_lt_i32 s2, 0
	s_cselect_b32 s2, 0, -1
	v_and_b32_e32 v0, s2, v0
	v_and_b32_e32 v1, s2, v1
	v_and_b32_e32 v2, s2, v2
	v_and_b32_e32 v3, s2, v3
	s_add_i32 s2, s5, -2
	s_cmp_lt_i32 s2, 0
	s_cselect_b32 s2, 0, -1
	v_and_b32_e32 v4, s2, v4
	v_and_b32_e32 v5, s2, v5
	v_and_b32_e32 v6, s2, v6
	v_and_b32_e32 v7, s2, v7
	s_add_i32 s2, s5, -1
	s_cmp_lt_i32 s2, 0
	s_cselect_b32 s2, 0, -1
	v_and_b32_e32 v8, s2, v8
	v_and_b32_e32 v9, s2, v9
	v_and_b32_e32 v10, s2, v10
	v_and_b32_e32 v11, s2, v11
.Lp2_nomask_even:
	s_waitcnt vmcnt(44)
	v_lshlrev_b32_e32 v196, 16, v0
	v_and_b32_e32 v197, 0xffff0000, v0
	v_lshlrev_b32_e32 v198, 16, v1
	v_and_b32_e32 v199, 0xffff0000, v1
	v_lshlrev_b32_e32 v200, 16, v2
	v_and_b32_e32 v201, 0xffff0000, v2
	v_lshlrev_b32_e32 v202, 16, v3
	v_and_b32_e32 v203, 0xffff0000, v3
	s_waitcnt vmcnt(43)
	v_lshlrev_b32_e32 v188, 16, v4
	v_and_b32_e32 v189, 0xffff0000, v4
	v_lshlrev_b32_e32 v190, 16, v5
	v_and_b32_e32 v191, 0xffff0000, v5
	v_lshlrev_b32_e32 v192, 16, v6
	v_and_b32_e32 v193, 0xffff0000, v6
	v_lshlrev_b32_e32 v194, 16, v7
	v_and_b32_e32 v195, 0xffff0000, v7
	v_pk_add_f32 v[196:197], v[196:197], v[188:189]
	v_pk_add_f32 v[198:199], v[198:199], v[190:191]
	v_pk_add_f32 v[200:201], v[200:201], v[192:193]
	v_pk_add_f32 v[202:203], v[202:203], v[194:195]
	s_waitcnt vmcnt(42)
	v_lshlrev_b32_e32 v180, 16, v8
	v_and_b32_e32 v181, 0xffff0000, v8
	v_lshlrev_b32_e32 v182, 16, v9
	v_and_b32_e32 v183, 0xffff0000, v9
	v_lshlrev_b32_e32 v184, 16, v10
	v_and_b32_e32 v185, 0xffff0000, v10
	v_lshlrev_b32_e32 v186, 16, v11
	v_and_b32_e32 v187, 0xffff0000, v11
	v_pk_fma_f32 v[180:181], v[196:197], v[218:219], v[180:181] op_sel_hi:[1,0,1]
	v_pk_fma_f32 v[182:183], v[198:199], v[218:219], v[182:183] op_sel_hi:[1,0,1]
	v_pk_fma_f32 v[184:185], v[200:201], v[218:219], v[184:185] op_sel_hi:[1,0,1]
	v_pk_fma_f32 v[186:187], v[202:203], v[218:219], v[186:187] op_sel_hi:[1,0,1]
	s_add_i32 s2, s5, 1
	v_min_u32_e32 v217, s2, v219
	v_cvt_f32_u32_e32 v217, v217
	v_rcp_f32_e32 v216, v217
	s_waitcnt vmcnt(41)
	v_lshlrev_b32_e32 v188, 16, v12
	v_and_b32_e32 v189, 0xffff0000, v12
	v_lshlrev_b32_e32 v190, 16, v13
	v_and_b32_e32 v191, 0xffff0000, v13
	v_lshlrev_b32_e32 v192, 16, v14
	v_and_b32_e32 v193, 0xffff0000, v14
	v_lshlrev_b32_e32 v194, 16, v15
	v_and_b32_e32 v195, 0xffff0000, v15
	v_pk_add_f32 v[180:181], v[180:181], v[188:189]
	v_pk_add_f32 v[182:183], v[182:183], v[190:191]
	v_pk_add_f32 v[184:185], v[184:185], v[192:193]
	v_pk_add_f32 v[186:187], v[186:187], v[194:195]
	v_pk_fma_f32 v[196:197], v[180:181], v[216:217], v[188:189] op_sel_hi:[1,0,1] neg_lo:[0,0,1] neg_hi:[0,0,1]
	v_pk_fma_f32 v[198:199], v[182:183], v[216:217], v[190:191] op_sel_hi:[1,0,1] neg_lo:[0,0,1] neg_hi:[0,0,1]
	v_pk_fma_f32 v[200:201], v[184:185], v[216:217], v[192:193] op_sel_hi:[1,0,1] neg_lo:[0,0,1] neg_hi:[0,0,1]
	v_pk_fma_f32 v[202:203], v[186:187], v[216:217], v[194:195] op_sel_hi:[1,0,1] neg_lo:[0,0,1] neg_hi:[0,0,1]
	v_cvt_pk_bf16_f32 v208, v196, v197
	v_cvt_pk_bf16_f32 v209, v198, v199
	v_cvt_pk_bf16_f32 v210, v200, v201
	v_cvt_pk_bf16_f32 v211, v202, v203
	global_store_dwordx4 v220, v[208:211], s[26:27]
	v_cndmask_b32_e64 v204, v8, v0, s[8:9]
	v_cndmask_b32_e64 v205, v9, v1, s[8:9]
	v_cndmask_b32_e64 v206, v10, v2, s[8:9]
	v_cndmask_b32_e64 v207, v11, v3, s[8:9]
	v_lshlrev_b32_e32 v196, 16, v204
	v_and_b32_e32 v197, 0xffff0000, v204
	v_lshlrev_b32_e32 v198, 16, v205
	v_and_b32_e32 v199, 0xffff0000, v205
	v_lshlrev_b32_e32 v200, 16, v206
	v_and_b32_e32 v201, 0xffff0000, v206
	v_lshlrev_b32_e32 v202, 16, v207
	v_and_b32_e32 v203, 0xffff0000, v207
	v_pk_add_f32 v[180:181], v[180:181], v[196:197] neg_lo:[0,1] neg_hi:[0,1]
	v_pk_add_f32 v[182:183], v[182:183], v[198:199] neg_lo:[0,1] neg_hi:[0,1]
	v_pk_add_f32 v[184:185], v[184:185], v[200:201] neg_lo:[0,1] neg_hi:[0,1]
	v_pk_add_f32 v[186:187], v[186:187], v[202:203] neg_lo:[0,1] neg_hi:[0,1]
	s_add_i32 s2, s5, 2
	v_min_u32_e32 v217, s2, v219
	v_cvt_f32_u32_e32 v217, v217
	v_rcp_f32_e32 v216, v217
	s_waitcnt vmcnt(41)
	v_lshlrev_b32_e32 v188, 16, v16
	v_and_b32_e32 v189, 0xffff0000, v16
	v_lshlrev_b32_e32 v190, 16, v17
	v_and_b32_e32 v191, 0xffff0000, v17
	v_lshlrev_b32_e32 v192, 16, v18
	v_and_b32_e32 v193, 0xffff0000, v18
	v_lshlrev_b32_e32 v194, 16, v19
	v_and_b32_e32 v195, 0xffff0000, v19
	v_pk_add_f32 v[180:181], v[180:181], v[188:189]
	v_pk_add_f32 v[182:183], v[182:183], v[190:191]
	v_pk_add_f32 v[184:185], v[184:185], v[192:193]
	v_pk_add_f32 v[186:187], v[186:187], v[194:195]
	v_pk_fma_f32 v[196:197], v[180:181], v[216:217], v[188:189] op_sel_hi:[1,0,1] neg_lo:[0,0,1] neg_hi:[0,0,1]
	v_pk_fma_f32 v[198:199], v[182:183], v[216:217], v[190:191] op_sel_hi:[1,0,1] neg_lo:[0,0,1] neg_hi:[0,0,1]
	v_pk_fma_f32 v[200:201], v[184:185], v[216:217], v[192:193] op_sel_hi:[1,0,1] neg_lo:[0,0,1] neg_hi:[0,0,1]
	v_pk_fma_f32 v[202:203], v[186:187], v[216:217], v[194:195] op_sel_hi:[1,0,1] neg_lo:[0,0,1] neg_hi:[0,0,1]
	v_cvt_pk_bf16_f32 v212, v196, v197
	v_cvt_pk_bf16_f32 v213, v198, v199
	v_cvt_pk_bf16_f32 v214, v200, v201
	v_cvt_pk_bf16_f32 v215, v202, v203
	s_add_u32 s20, s26, 0x1000
	s_addc_u32 s21, s27, 0
	global_store_dwordx4 v220, v[212:215], s[20:21]
	v_cndmask_b32_e64 v204, v12, v4, s[8:9]
	v_cndmask_b32_e64 v205, v13, v5, s[8:9]
	v_cndmask_b32_e64 v206, v14, v6, s[8:9]
	v_cndmask_b32_e64 v207, v15, v7, s[8:9]
	v_lshlrev_b32_e32 v196, 16, v204
	v_and_b32_e32 v197, 0xffff0000, v204
	v_lshlrev_b32_e32 v198, 16, v205
	v_and_b32_e32 v199, 0xffff0000, v205
	v_lshlrev_b32_e32 v200, 16, v206
	v_and_b32_e32 v201, 0xffff0000, v206
	v_lshlrev_b32_e32 v202, 16, v207
	v_and_b32_e32 v203, 0xffff0000, v207
	v_pk_add_f32 v[180:181], v[180:181], v[196:197] neg_lo:[0,1] neg_hi:[0,1]
	v_pk_add_f32 v[182:183], v[182:183], v[198:199] neg_lo:[0,1] neg_hi:[0,1]
	v_pk_add_f32 v[184:185], v[184:185], v[200:201] neg_lo:[0,1] neg_hi:[0,1]
	v_pk_add_f32 v[186:187], v[186:187], v[202:203] neg_lo:[0,1] neg_hi:[0,1]
	s_add_i32 s2, s5, 3
	v_min_u32_e32 v217, s2, v219
	v_cvt_f32_u32_e32 v217, v217
	v_rcp_f32_e32 v216, v217
	s_waitcnt vmcnt(41)
	v_lshlrev_b32_e32 v188, 16, v20
	v_and_b32_e32 v189, 0xffff0000, v20
	v_lshlrev_b32_e32 v190, 16, v21
	v_and_b32_e32 v191, 0xffff0000, v21
	v_lshlrev_b32_e32 v192, 16, v22
	v_and_b32_e32 v193, 0xffff0000, v22
	v_lshlrev_b32_e32 v194, 16, v23
	v_and_b32_e32 v195, 0xffff0000, v23
	v_pk_add_f32 v[180:181], v[180:181], v[188:189]
	v_pk_add_f32 v[182:183], v[182:183], v[190:191]
	v_pk_add_f32 v[184:185], v[184:185], v[192:193]
	v_pk_add_f32 v[186:187], v[186:187], v[194:195]
	v_pk_fma_f32 v[196:197], v[180:181], v[216:217], v[188:189] op_sel_hi:[1,0,1] neg_lo:[0,0,1] neg_hi:[0,0,1]
	v_pk_fma_f32 v[198:199], v[182:183], v[216:217], v[190:191] op_sel_hi:[1,0,1] neg_lo:[0,0,1] neg_hi:[0,0,1]
	v_pk_fma_f32 v[200:201], v[184:185], v[216:217], v[192:193] op_sel_hi:[1,0,1] neg_lo:[0,0,1] neg_hi:[0,0,1]
	v_pk_fma_f32 v[202:203], v[186:187], v[216:217], v[194:195] op_sel_hi:[1,0,1] neg_lo:[0,0,1] neg_hi:[0,0,1]
	v_cvt_pk_bf16_f32 v208, v196, v197
	v_cvt_pk_bf16_f32 v209, v198, v199
	v_cvt_pk_bf16_f32 v210, v200, v201
	v_cvt_pk_bf16_f32 v211, v202, v203
	s_add_u32 s20, s26, 0x2000
	s_addc_u32 s21, s27, 0
	global_store_dwordx4 v220, v[208:211], s[20:21]
	v_cndmask_b32_e64 v204, v16, v8, s[8:9]
	v_cndmask_b32_e64 v205, v17, v9, s[8:9]
	v_cndmask_b32_e64 v206, v18, v10, s[8:9]
	v_cndmask_b32_e64 v207, v19, v11, s[8:9]
	v_lshlrev_b32_e32 v196, 16, v204
	v_and_b32_e32 v197, 0xffff0000, v204
	v_lshlrev_b32_e32 v198, 16, v205
	v_and_b32_e32 v199, 0xffff0000, v205
	v_lshlrev_b32_e32 v200, 16, v206
	v_and_b32_e32 v201, 0xffff0000, v206
	v_lshlrev_b32_e32 v202, 16, v207
	v_and_b32_e32 v203, 0xffff0000, v207
	v_pk_add_f32 v[180:181], v[180:181], v[196:197] neg_lo:[0,1] neg_hi:[0,1]
	v_pk_add_f32 v[182:183], v[182:183], v[198:199] neg_lo:[0,1] neg_hi:[0,1]
	v_pk_add_f32 v[184:185], v[184:185], v[200:201] neg_lo:[0,1] neg_hi:[0,1]
	v_pk_add_f32 v[186:187], v[186:187], v[202:203] neg_lo:[0,1] neg_hi:[0,1]
	s_add_i32 s2, s5, 4
	v_min_u32_e32 v217, s2, v219
	v_cvt_f32_u32_e32 v217, v217
	v_rcp_f32_e32 v216, v217
	s_waitcnt vmcnt(41)
	v_lshlrev_b32_e32 v188, 16, v24
	v_and_b32_e32 v189, 0xffff0000, v24
	v_lshlrev_b32_e32 v190, 16, v25
	v_and_b32_e32 v191, 0xffff0000, v25
	v_lshlrev_b32_e32 v192, 16, v26
	v_and_b32_e32 v193, 0xffff0000, v26
	v_lshlrev_b32_e32 v194, 16, v27
	v_and_b32_e32 v195, 0xffff0000, v27
	v_pk_add_f32 v[180:181], v[180:181], v[188:189]
	v_pk_add_f32 v[182:183], v[182:183], v[190:191]
	v_pk_add_f32 v[184:185], v[184:185], v[192:193]
	v_pk_add_f32 v[186:187], v[186:187], v[194:195]
	v_pk_fma_f32 v[196:197], v[180:181], v[216:217], v[188:189] op_sel_hi:[1,0,1] neg_lo:[0,0,1] neg_hi:[0,0,1]
	v_pk_fma_f32 v[198:199], v[182:183], v[216:217], v[190:191] op_sel_hi:[1,0,1] neg_lo:[0,0,1] neg_hi:[0,0,1]
	v_pk_fma_f32 v[200:201], v[184:185], v[216:217], v[192:193] op_sel_hi:[1,0,1] neg_lo:[0,0,1] neg_hi:[0,0,1]
	v_pk_fma_f32 v[202:203], v[186:187], v[216:217], v[194:195] op_sel_hi:[1,0,1] neg_lo:[0,0,1] neg_hi:[0,0,1]
	v_cvt_pk_bf16_f32 v212, v196, v197
	v_cvt_pk_bf16_f32 v213, v198, v199
	v_cvt_pk_bf16_f32 v214, v200, v201
	v_cvt_pk_bf16_f32 v215, v202, v203
	s_add_u32 s20, s26, 0x3000
	s_addc_u32 s21, s27, 0
	global_store_dwordx4 v220, v[212:215], s[20:21]
	v_cndmask_b32_e64 v204, v20, v12, s[8:9]
	v_cndmask_b32_e64 v205, v21, v13, s[8:9]
	v_cndmask_b32_e64 v206, v22, v14, s[8:9]
	v_cndmask_b32_e64 v207, v23, v15, s[8:9]
	v_lshlrev_b32_e32 v196, 16, v204
	v_and_b32_e32 v197, 0xffff0000, v204
	v_lshlrev_b32_e32 v198, 16, v205
	v_and_b32_e32 v199, 0xffff0000, v205
	v_lshlrev_b32_e32 v200, 16, v206
	v_and_b32_e32 v201, 0xffff0000, v206
	v_lshlrev_b32_e32 v202, 16, v207
	v_and_b32_e32 v203, 0xffff0000, v207
	v_pk_add_f32 v[180:181], v[180:181], v[196:197] neg_lo:[0,1] neg_hi:[0,1]
	v_pk_add_f32 v[182:183], v[182:183], v[198:199] neg_lo:[0,1] neg_hi:[0,1]
	v_pk_add_f32 v[184:185], v[184:185], v[200:201] neg_lo:[0,1] neg_hi:[0,1]
	v_pk_add_f32 v[186:187], v[186:187], v[202:203] neg_lo:[0,1] neg_hi:[0,1]
	s_add_i32 s2, s5, 5
	v_min_u32_e32 v217, s2, v219
	v_cvt_f32_u32_e32 v217, v217
	v_rcp_f32_e32 v216, v217
	s_waitcnt vmcnt(41)
	v_lshlrev_b32_e32 v188, 16, v28
	v_and_b32_e32 v189, 0xffff0000, v28
	v_lshlrev_b32_e32 v190, 16, v29
	v_and_b32_e32 v191, 0xffff0000, v29
	v_lshlrev_b32_e32 v192, 16, v30
	v_and_b32_e32 v193, 0xffff0000, v30
	v_lshlrev_b32_e32 v194, 16, v31
	v_and_b32_e32 v195, 0xffff0000, v31
	v_pk_add_f32 v[180:181], v[180:181], v[188:189]
	v_pk_add_f32 v[182:183], v[182:183], v[190:191]
	v_pk_add_f32 v[184:185], v[184:185], v[192:193]
	v_pk_add_f32 v[186:187], v[186:187], v[194:195]
	v_pk_fma_f32 v[196:197], v[180:181], v[216:217], v[188:189] op_sel_hi:[1,0,1] neg_lo:[0,0,1] neg_hi:[0,0,1]
	v_pk_fma_f32 v[198:199], v[182:183], v[216:217], v[190:191] op_sel_hi:[1,0,1] neg_lo:[0,0,1] neg_hi:[0,0,1]
	v_pk_fma_f32 v[200:201], v[184:185], v[216:217], v[192:193] op_sel_hi:[1,0,1] neg_lo:[0,0,1] neg_hi:[0,0,1]
	v_pk_fma_f32 v[202:203], v[186:187], v[216:217], v[194:195] op_sel_hi:[1,0,1] neg_lo:[0,0,1] neg_hi:[0,0,1]
	v_cvt_pk_bf16_f32 v208, v196, v197
	v_cvt_pk_bf16_f32 v209, v198, v199
	v_cvt_pk_bf16_f32 v210, v200, v201
	v_cvt_pk_bf16_f32 v211, v202, v203
	s_add_u32 s20, s26, 0x4000
	s_addc_u32 s21, s27, 0
	global_store_dwordx4 v220, v[208:211], s[20:21]
	v_cndmask_b32_e64 v204, v24, v16, s[8:9]
	v_cndmask_b32_e64 v205, v25, v17, s[8:9]
	v_cndmask_b32_e64 v206, v26, v18, s[8:9]
	v_cndmask_b32_e64 v207, v27, v19, s[8:9]
	v_lshlrev_b32_e32 v196, 16, v204
	v_and_b32_e32 v197, 0xffff0000, v204
	v_lshlrev_b32_e32 v198, 16, v205
	v_and_b32_e32 v199, 0xffff0000, v205
	v_lshlrev_b32_e32 v200, 16, v206
	v_and_b32_e32 v201, 0xffff0000, v206
	v_lshlrev_b32_e32 v202, 16, v207
	v_and_b32_e32 v203, 0xffff0000, v207
	v_pk_add_f32 v[180:181], v[180:181], v[196:197] neg_lo:[0,1] neg_hi:[0,1]
	v_pk_add_f32 v[182:183], v[182:183], v[198:199] neg_lo:[0,1] neg_hi:[0,1]
	v_pk_add_f32 v[184:185], v[184:185], v[200:201] neg_lo:[0,1] neg_hi:[0,1]
	v_pk_add_f32 v[186:187], v[186:187], v[202:203] neg_lo:[0,1] neg_hi:[0,1]
	s_add_i32 s2, s5, 6
	v_min_u32_e32 v217, s2, v219
	v_cvt_f32_u32_e32 v217, v217
	v_rcp_f32_e32 v216, v217
	s_waitcnt vmcnt(41)
	v_lshlrev_b32_e32 v188, 16, v32
	v_and_b32_e32 v189, 0xffff0000, v32
	v_lshlrev_b32_e32 v190, 16, v33
	v_and_b32_e32 v191, 0xffff0000, v33
	v_lshlrev_b32_e32 v192, 16, v34
	v_and_b32_e32 v193, 0xffff0000, v34
	v_lshlrev_b32_e32 v194, 16, v35
	v_and_b32_e32 v195, 0xffff0000, v35
	v_pk_add_f32 v[180:181], v[180:181], v[188:189]
	v_pk_add_f32 v[182:183], v[182:183], v[190:191]
	v_pk_add_f32 v[184:185], v[184:185], v[192:193]
	v_pk_add_f32 v[186:187], v[186:187], v[194:195]
	v_pk_fma_f32 v[196:197], v[180:181], v[216:217], v[188:189] op_sel_hi:[1,0,1] neg_lo:[0,0,1] neg_hi:[0,0,1]
	v_pk_fma_f32 v[198:199], v[182:183], v[216:217], v[190:191] op_sel_hi:[1,0,1] neg_lo:[0,0,1] neg_hi:[0,0,1]
	v_pk_fma_f32 v[200:201], v[184:185], v[216:217], v[192:193] op_sel_hi:[1,0,1] neg_lo:[0,0,1] neg_hi:[0,0,1]
	v_pk_fma_f32 v[202:203], v[186:187], v[216:217], v[194:195] op_sel_hi:[1,0,1] neg_lo:[0,0,1] neg_hi:[0,0,1]
	v_cvt_pk_bf16_f32 v212, v196, v197
	v_cvt_pk_bf16_f32 v213, v198, v199
	v_cvt_pk_bf16_f32 v214, v200, v201
	v_cvt_pk_bf16_f32 v215, v202, v203
	s_add_u32 s20, s26, 0x5000
	s_addc_u32 s21, s27, 0
	global_store_dwordx4 v220, v[212:215], s[20:21]
	v_cndmask_b32_e64 v204, v28, v20, s[8:9]
	v_cndmask_b32_e64 v205, v29, v21, s[8:9]
	v_cndmask_b32_e64 v206, v30, v22, s[8:9]
	v_cndmask_b32_e64 v207, v31, v23, s[8:9]
	v_lshlrev_b32_e32 v196, 16, v204
	v_and_b32_e32 v197, 0xffff0000, v204
	v_lshlrev_b32_e32 v198, 16, v205
	v_and_b32_e32 v199, 0xffff0000, v205
	v_lshlrev_b32_e32 v200, 16, v206
	v_and_b32_e32 v201, 0xffff0000, v206
	v_lshlrev_b32_e32 v202, 16, v207
	v_and_b32_e32 v203, 0xffff0000, v207
	v_pk_add_f32 v[180:181], v[180:181], v[196:197] neg_lo:[0,1] neg_hi:[0,1]
	v_pk_add_f32 v[182:183], v[182:183], v[198:199] neg_lo:[0,1] neg_hi:[0,1]
	v_pk_add_f32 v[184:185], v[184:185], v[200:201] neg_lo:[0,1] neg_hi:[0,1]
	v_pk_add_f32 v[186:187], v[186:187], v[202:203] neg_lo:[0,1] neg_hi:[0,1]
	s_add_i32 s2, s5, 7
	v_min_u32_e32 v217, s2, v219
	v_cvt_f32_u32_e32 v217, v217
	v_rcp_f32_e32 v216, v217
	s_waitcnt vmcnt(41)
	v_lshlrev_b32_e32 v188, 16, v36
	v_and_b32_e32 v189, 0xffff0000, v36
	v_lshlrev_b32_e32 v190, 16, v37
	v_and_b32_e32 v191, 0xffff0000, v37
	v_lshlrev_b32_e32 v192, 16, v38
	v_and_b32_e32 v193, 0xffff0000, v38
	v_lshlrev_b32_e32 v194, 16, v39
	v_and_b32_e32 v195, 0xffff0000, v39
	v_pk_add_f32 v[180:181], v[180:181], v[188:189]
	v_pk_add_f32 v[182:183], v[182:183], v[190:191]
	v_pk_add_f32 v[184:185], v[184:185], v[192:193]
	v_pk_add_f32 v[186:187], v[186:187], v[194:195]
	v_pk_fma_f32 v[196:197], v[180:181], v[216:217], v[188:189] op_sel_hi:[1,0,1] neg_lo:[0,0,1] neg_hi:[0,0,1]
	v_pk_fma_f32 v[198:199], v[182:183], v[216:217], v[190:191] op_sel_hi:[1,0,1] neg_lo:[0,0,1] neg_hi:[0,0,1]
	v_pk_fma_f32 v[200:201], v[184:185], v[216:217], v[192:193] op_sel_hi:[1,0,1] neg_lo:[0,0,1] neg_hi:[0,0,1]
	v_pk_fma_f32 v[202:203], v[186:187], v[216:217], v[194:195] op_sel_hi:[1,0,1] neg_lo:[0,0,1] neg_hi:[0,0,1]
	v_cvt_pk_bf16_f32 v208, v196, v197
	v_cvt_pk_bf16_f32 v209, v198, v199
	v_cvt_pk_bf16_f32 v210, v200, v201
	v_cvt_pk_bf16_f32 v211, v202, v203
	s_add_u32 s20, s26, 0x6000
	s_addc_u32 s21, s27, 0
	global_store_dwordx4 v220, v[208:211], s[20:21]
	v_cndmask_b32_e64 v204, v32, v24, s[8:9]
	v_cndmask_b32_e64 v205, v33, v25, s[8:9]
	v_cndmask_b32_e64 v206, v34, v26, s[8:9]
	v_cndmask_b32_e64 v207, v35, v27, s[8:9]
	v_lshlrev_b32_e32 v196, 16, v204
	v_and_b32_e32 v197, 0xffff0000, v204
	v_lshlrev_b32_e32 v198, 16, v205
	v_and_b32_e32 v199, 0xffff0000, v205
	v_lshlrev_b32_e32 v200, 16, v206
	v_and_b32_e32 v201, 0xffff0000, v206
	v_lshlrev_b32_e32 v202, 16, v207
	v_and_b32_e32 v203, 0xffff0000, v207
	v_pk_add_f32 v[180:181], v[180:181], v[196:197] neg_lo:[0,1] neg_hi:[0,1]
	v_pk_add_f32 v[182:183], v[182:183], v[198:199] neg_lo:[0,1] neg_hi:[0,1]
	v_pk_add_f32 v[184:185], v[184:185], v[200:201] neg_lo:[0,1] neg_hi:[0,1]
	v_pk_add_f32 v[186:187], v[186:187], v[202:203] neg_lo:[0,1] neg_hi:[0,1]
	s_add_i32 s2, s5, 8
	v_min_u32_e32 v217, s2, v219
	v_cvt_f32_u32_e32 v217, v217
	v_rcp_f32_e32 v216, v217
	s_waitcnt vmcnt(41)
	v_lshlrev_b32_e32 v188, 16, v40
	v_and_b32_e32 v189, 0xffff0000, v40
	v_lshlrev_b32_e32 v190, 16, v41
	v_and_b32_e32 v191, 0xffff0000, v41
	v_lshlrev_b32_e32 v192, 16, v42
	v_and_b32_e32 v193, 0xffff0000, v42
	v_lshlrev_b32_e32 v194, 16, v43
	v_and_b32_e32 v195, 0xffff0000, v43
	v_pk_add_f32 v[180:181], v[180:181], v[188:189]
	v_pk_add_f32 v[182:183], v[182:183], v[190:191]
	v_pk_add_f32 v[184:185], v[184:185], v[192:193]
	v_pk_add_f32 v[186:187], v[186:187], v[194:195]
	v_pk_fma_f32 v[196:197], v[180:181], v[216:217], v[188:189] op_sel_hi:[1,0,1] neg_lo:[0,0,1] neg_hi:[0,0,1]
	v_pk_fma_f32 v[198:199], v[182:183], v[216:217], v[190:191] op_sel_hi:[1,0,1] neg_lo:[0,0,1] neg_hi:[0,0,1]
	v_pk_fma_f32 v[200:201], v[184:185], v[216:217], v[192:193] op_sel_hi:[1,0,1] neg_lo:[0,0,1] neg_hi:[0,0,1]
	v_pk_fma_f32 v[202:203], v[186:187], v[216:217], v[194:195] op_sel_hi:[1,0,1] neg_lo:[0,0,1] neg_hi:[0,0,1]
	v_cvt_pk_bf16_f32 v212, v196, v197
	v_cvt_pk_bf16_f32 v213, v198, v199
	v_cvt_pk_bf16_f32 v214, v200, v201
	v_cvt_pk_bf16_f32 v215, v202, v203
	s_add_u32 s20, s26, 0x7000
	s_addc_u32 s21, s27, 0
	global_store_dwordx4 v220, v[212:215], s[20:21]
	s_waitcnt vmcnt(26)
	s_add_i32 s2, s5, -2
	s_cmp_lt_i32 s2, 0
	s_cselect_b32 s2, 0, -1
	v_and_b32_e32 v148, s2, v148
	v_and_b32_e32 v149, s2, v149
	v_and_b32_e32 v150, s2, v150
	v_and_b32_e32 v151, s2, v151
	v_lshlrev_b32_e32 v180, 16, v148
	v_and_b32_e32 v181, 0xffff0000, v148
	v_lshlrev_b32_e32 v182, 16, v149
	v_and_b32_e32 v183, 0xffff0000, v149
	v_lshlrev_b32_e32 v184, 16, v150
	v_and_b32_e32 v185, 0xffff0000, v150
	v_lshlrev_b32_e32 v186, 16, v151
	v_and_b32_e32 v187, 0xffff0000, v151
	v_lshlrev_b32_e32 v188, 16, v152
	v_and_b32_e32 v189, 0xffff0000, v152
	v_lshlrev_b32_e32 v190, 16, v153
	v_and_b32_e32 v191, 0xffff0000, v153
	v_lshlrev_b32_e32 v192, 16, v154
	v_and_b32_e32 v193, 0xffff0000, v154
	v_lshlrev_b32_e32 v194, 16, v155
	v_and_b32_e32 v195, 0xffff0000, v155
	v_pk_mul_f32 v[0:1], v[180:181], v[188:189]
	v_pk_mul_f32 v[2:3], v[182:183], v[190:191]
	v_pk_mul_f32 v[4:5], v[184:185], v[192:193]
	v_pk_mul_f32 v[6:7], v[186:187], v[194:195]
	s_waitcnt vmcnt(24)
	s_add_i32 s2, s5, -1
	s_cmp_lt_i32 s2, 0
	s_cselect_b32 s2, 0, -1
	v_and_b32_e32 v156, s2, v156
	v_and_b32_e32 v157, s2, v157
	v_and_b32_e32 v158, s2, v158
	v_and_b32_e32 v159, s2, v159
	v_lshlrev_b32_e32 v180, 16, v156
	v_and_b32_e32 v181, 0xffff0000, v156
	v_lshlrev_b32_e32 v182, 16, v157
	v_and_b32_e32 v183, 0xffff0000, v157
	v_lshlrev_b32_e32 v184, 16, v158
	v_and_b32_e32 v185, 0xffff0000, v158
	v_lshlrev_b32_e32 v186, 16, v159
	v_and_b32_e32 v187, 0xffff0000, v159
	v_lshlrev_b32_e32 v188, 16, v160
	v_and_b32_e32 v189, 0xffff0000, v160
	v_lshlrev_b32_e32 v190, 16, v161
	v_and_b32_e32 v191, 0xffff0000, v161
	v_lshlrev_b32_e32 v192, 16, v162
	v_and_b32_e32 v193, 0xffff0000, v162
	v_lshlrev_b32_e32 v194, 16, v163
	v_and_b32_e32 v195, 0xffff0000, v163
	v_pk_mul_f32 v[8:9], v[180:181], v[188:189]
	v_pk_mul_f32 v[10:11], v[182:183], v[190:191]
	v_pk_mul_f32 v[12:13], v[184:185], v[192:193]
	v_pk_mul_f32 v[14:15], v[186:187], v[194:195]
	s_waitcnt vmcnt(22)
	v_lshlrev_b32_e32 v180, 16, v164
	v_and_b32_e32 v181, 0xffff0000, v164
	v_lshlrev_b32_e32 v182, 16, v165
	v_and_b32_e32 v183, 0xffff0000, v165
	v_lshlrev_b32_e32 v184, 16, v166
	v_and_b32_e32 v185, 0xffff0000, v166
	v_lshlrev_b32_e32 v186, 16, v167
	v_and_b32_e32 v187, 0xffff0000, v167
	v_lshlrev_b32_e32 v188, 16, v168
	v_and_b32_e32 v189, 0xffff0000, v168
	v_lshlrev_b32_e32 v190, 16, v169
	v_and_b32_e32 v191, 0xffff0000, v169
	v_lshlrev_b32_e32 v192, 16, v170
	v_and_b32_e32 v193, 0xffff0000, v170
	v_lshlrev_b32_e32 v194, 16, v171
	v_and_b32_e32 v195, 0xffff0000, v171
	v_pk_mul_f32 v[16:17], v[180:181], v[188:189]
	v_pk_mul_f32 v[18:19], v[182:183], v[190:191]
	v_pk_mul_f32 v[20:21], v[184:185], v[192:193]
	v_pk_mul_f32 v[22:23], v[186:187], v[194:195]
	v_pk_mul_f32 v[24:25], v[92:93], v[0:1]
	v_pk_mul_f32 v[26:27], v[94:95], v[2:3]
	v_pk_mul_f32 v[28:29], v[96:97], v[4:5]
	v_pk_mul_f32 v[30:31], v[98:99], v[6:7]
	v_pk_fma_f32 v[24:25], v[100:101], v[8:9], v[24:25]
	v_pk_fma_f32 v[26:27], v[102:103], v[10:11], v[26:27]
	v_pk_fma_f32 v[28:29], v[104:105], v[12:13], v[28:29]
	v_pk_fma_f32 v[30:31], v[106:107], v[14:15], v[30:31]
	v_pk_fma_f32 v[24:25], v[108:109], v[16:17], v[24:25]
	v_pk_fma_f32 v[26:27], v[110:111], v[18:19], v[26:27]
	v_pk_fma_f32 v[28:29], v[112:113], v[20:21], v[28:29]
	v_pk_fma_f32 v[30:31], v[114:115], v[22:23], v[30:31]
	s_waitcnt vmcnt(35)
	v_lshlrev_b32_e32 v196, 16, v116
	v_and_b32_e32 v197, 0xffff0000, v116
	v_lshlrev_b32_e32 v198, 16, v117
	v_and_b32_e32 v199, 0xffff0000, v117
	v_lshlrev_b32_e32 v200, 16, v118
	v_and_b32_e32 v201, 0xffff0000, v118
	v_lshlrev_b32_e32 v202, 16, v119
	v_and_b32_e32 v203, 0xffff0000, v119
	v_pk_mul_f32 v[24:25], v[24:25], v[196:197]
	v_pk_mul_f32 v[26:27], v[26:27], v[198:199]
	v_pk_mul_f32 v[28:29], v[28:29], v[200:201]
	v_pk_mul_f32 v[30:31], v[30:31], v[202:203]
	v_cvt_pk_bf16_f32 v208, v24, v25
	v_cvt_pk_bf16_f32 v209, v26, v27
	v_cvt_pk_bf16_f32 v210, v28, v29
	v_cvt_pk_bf16_f32 v211, v30, v31
	global_store_dwordx4 v220, v[208:211], s[26:27] offset:2048
	s_waitcnt vmcnt(21)
	v_lshlrev_b32_e32 v180, 16, v172
	v_and_b32_e32 v181, 0xffff0000, v172
	v_lshlrev_b32_e32 v182, 16, v173
	v_and_b32_e32 v183, 0xffff0000, v173
	v_lshlrev_b32_e32 v184, 16, v174
	v_and_b32_e32 v185, 0xffff0000, v174
	v_lshlrev_b32_e32 v186, 16, v175
	v_and_b32_e32 v187, 0xffff0000, v175
	v_lshlrev_b32_e32 v188, 16, v176
	v_and_b32_e32 v189, 0xffff0000, v176
	v_lshlrev_b32_e32 v190, 16, v177
	v_and_b32_e32 v191, 0xffff0000, v177
	v_lshlrev_b32_e32 v192, 16, v178
	v_and_b32_e32 v193, 0xffff0000, v178
	v_lshlrev_b32_e32 v194, 16, v179
	v_and_b32_e32 v195, 0xffff0000, v179
	v_pk_mul_f32 v[0:1], v[180:181], v[188:189]
	v_pk_mul_f32 v[2:3], v[182:183], v[190:191]
	v_pk_mul_f32 v[4:5], v[184:185], v[192:193]
	v_pk_mul_f32 v[6:7], v[186:187], v[194:195]
	v_pk_mul_f32 v[24:25], v[92:93], v[8:9]
	v_pk_mul_f32 v[26:27], v[94:95], v[10:11]
	v_pk_mul_f32 v[28:29], v[96:97], v[12:13]
	v_pk_mul_f32 v[30:31], v[98:99], v[14:15]
	v_pk_fma_f32 v[24:25], v[100:101], v[16:17], v[24:25]
	v_pk_fma_f32 v[26:27], v[102:103], v[18:19], v[26:27]
	v_pk_fma_f32 v[28:29], v[104:105], v[20:21], v[28:29]
	v_pk_fma_f32 v[30:31], v[106:107], v[22:23], v[30:31]
	v_pk_fma_f32 v[24:25], v[108:109], v[0:1], v[24:25]
	v_pk_fma_f32 v[26:27], v[110:111], v[2:3], v[26:27]
	v_pk_fma_f32 v[28:29], v[112:113], v[4:5], v[28:29]
	v_pk_fma_f32 v[30:31], v[114:115], v[6:7], v[30:31]
	s_waitcnt vmcnt(35)
	v_lshlrev_b32_e32 v196, 16, v120
	v_and_b32_e32 v197, 0xffff0000, v120
	v_lshlrev_b32_e32 v198, 16, v121
	v_and_b32_e32 v199, 0xffff0000, v121
	v_lshlrev_b32_e32 v200, 16, v122
	v_and_b32_e32 v201, 0xffff0000, v122
	v_lshlrev_b32_e32 v202, 16, v123
	v_and_b32_e32 v203, 0xffff0000, v123
	v_pk_mul_f32 v[24:25], v[24:25], v[196:197]
	v_pk_mul_f32 v[26:27], v[26:27], v[198:199]
	v_pk_mul_f32 v[28:29], v[28:29], v[200:201]
	v_pk_mul_f32 v[30:31], v[30:31], v[202:203]
	v_cvt_pk_bf16_f32 v212, v24, v25
	v_cvt_pk_bf16_f32 v213, v26, v27
	v_cvt_pk_bf16_f32 v214, v28, v29
	v_cvt_pk_bf16_f32 v215, v30, v31
	s_add_u32 s20, s26, 0x1000
	s_addc_u32 s21, s27, 0
	global_store_dwordx4 v220, v[212:215], s[20:21] offset:2048
	s_waitcnt vmcnt(20)
	v_lshlrev_b32_e32 v180, 16, v44
	v_and_b32_e32 v181, 0xffff0000, v44
	v_lshlrev_b32_e32 v182, 16, v45
	v_and_b32_e32 v183, 0xffff0000, v45
	v_lshlrev_b32_e32 v184, 16, v46
	v_and_b32_e32 v185, 0xffff0000, v46
	v_lshlrev_b32_e32 v186, 16, v47
	v_and_b32_e32 v187, 0xffff0000, v47
	v_lshlrev_b32_e32 v188, 16, v48
	v_and_b32_e32 v189, 0xffff0000, v48
	v_lshlrev_b32_e32 v190, 16, v49
	v_and_b32_e32 v191, 0xffff0000, v49
	v_lshlrev_b32_e32 v192, 16, v50
	v_and_b32_e32 v193, 0xffff0000, v50
	v_lshlrev_b32_e32 v194, 16, v51
	v_and_b32_e32 v195, 0xffff0000, v51
	v_pk_mul_f32 v[8:9], v[180:181], v[188:189]
	v_pk_mul_f32 v[10:11], v[182:183], v[190:191]
	v_pk_mul_f32 v[12:13], v[184:185], v[192:193]
	v_pk_mul_f32 v[14:15], v[186:187], v[194:195]
	v_pk_mul_f32 v[24:25], v[92:93], v[16:17]
	v_pk_mul_f32 v[26:27], v[94:95], v[18:19]
	v_pk_mul_f32 v[28:29], v[96:97], v[20:21]
	v_pk_mul_f32 v[30:31], v[98:99], v[22:23]
	v_pk_fma_f32 v[24:25], v[100:101], v[0:1], v[24:25]
	v_pk_fma_f32 v[26:27], v[102:103], v[2:3], v[26:27]
	v_pk_fma_f32 v[28:29], v[104:105], v[4:5], v[28:29]
	v_pk_fma_f32 v[30:31], v[106:107], v[6:7], v[30:31]
	v_pk_fma_f32 v[24:25], v[108:109], v[8:9], v[24:25]
	v_pk_fma_f32 v[26:27], v[110:111], v[10:11], v[26:27]
	v_pk_fma_f32 v[28:29], v[112:113], v[12:13], v[28:29]
	v_pk_fma_f32 v[30:31], v[114:115], v[14:15], v[30:31]
	s_waitcnt vmcnt(35)
	v_lshlrev_b32_e32 v196, 16, v124
	v_and_b32_e32 v197, 0xffff0000, v124
	v_lshlrev_b32_e32 v198, 16, v125
	v_and_b32_e32 v199, 0xffff0000, v125
	v_lshlrev_b32_e32 v200, 16, v126
	v_and_b32_e32 v201, 0xffff0000, v126
	v_lshlrev_b32_e32 v202, 16, v127
	v_and_b32_e32 v203, 0xffff0000, v127
	v_pk_mul_f32 v[24:25], v[24:25], v[196:197]
	v_pk_mul_f32 v[26:27], v[26:27], v[198:199]
	v_pk_mul_f32 v[28:29], v[28:29], v[200:201]
	v_pk_mul_f32 v[30:31], v[30:31], v[202:203]
	v_cvt_pk_bf16_f32 v208, v24, v25
	v_cvt_pk_bf16_f32 v209, v26, v27
	v_cvt_pk_bf16_f32 v210, v28, v29
	v_cvt_pk_bf16_f32 v211, v30, v31
	s_add_u32 s20, s26, 0x2000
	s_addc_u32 s21, s27, 0
	global_store_dwordx4 v220, v[208:211], s[20:21] offset:2048
	s_waitcnt vmcnt(19)
	v_lshlrev_b32_e32 v180, 16, v52
	v_and_b32_e32 v181, 0xffff0000, v52
	v_lshlrev_b32_e32 v182, 16, v53
	v_and_b32_e32 v183, 0xffff0000, v53
	v_lshlrev_b32_e32 v184, 16, v54
	v_and_b32_e32 v185, 0xffff0000, v54
	v_lshlrev_b32_e32 v186, 16, v55
	v_and_b32_e32 v187, 0xffff0000, v55
	v_lshlrev_b32_e32 v188, 16, v56
	v_and_b32_e32 v189, 0xffff0000, v56
	v_lshlrev_b32_e32 v190, 16, v57
	v_and_b32_e32 v191, 0xffff0000, v57
	v_lshlrev_b32_e32 v192, 16, v58
	v_and_b32_e32 v193, 0xffff0000, v58
	v_lshlrev_b32_e32 v194, 16, v59
	v_and_b32_e32 v195, 0xffff0000, v59
	v_pk_mul_f32 v[16:17], v[180:181], v[188:189]
	v_pk_mul_f32 v[18:19], v[182:183], v[190:191]
	v_pk_mul_f32 v[20:21], v[184:185], v[192:193]
	v_pk_mul_f32 v[22:23], v[186:187], v[194:195]
	v_pk_mul_f32 v[24:25], v[92:93], v[0:1]
	v_pk_mul_f32 v[26:27], v[94:95], v[2:3]
	v_pk_mul_f32 v[28:29], v[96:97], v[4:5]
	v_pk_mul_f32 v[30:31], v[98:99], v[6:7]
	v_pk_fma_f32 v[24:25], v[100:101], v[8:9], v[24:25]
	v_pk_fma_f32 v[26:27], v[102:103], v[10:11], v[26:27]
	v_pk_fma_f32 v[28:29], v[104:105], v[12:13], v[28:29]
	v_pk_fma_f32 v[30:31], v[106:107], v[14:15], v[30:31]
	v_pk_fma_f32 v[24:25], v[108:109], v[16:17], v[24:25]
	v_pk_fma_f32 v[26:27], v[110:111], v[18:19], v[26:27]
	v_pk_fma_f32 v[28:29], v[112:113], v[20:21], v[28:29]
	v_pk_fma_f32 v[30:31], v[114:115], v[22:23], v[30:31]
	s_waitcnt vmcnt(35)
	v_lshlrev_b32_e32 v196, 16, v128
	v_and_b32_e32 v197, 0xffff0000, v128
	v_lshlrev_b32_e32 v198, 16, v129
	v_and_b32_e32 v199, 0xffff0000, v129
	v_lshlrev_b32_e32 v200, 16, v130
	v_and_b32_e32 v201, 0xffff0000, v130
	v_lshlrev_b32_e32 v202, 16, v131
	v_and_b32_e32 v203, 0xffff0000, v131
	v_pk_mul_f32 v[24:25], v[24:25], v[196:197]
	v_pk_mul_f32 v[26:27], v[26:27], v[198:199]
	v_pk_mul_f32 v[28:29], v[28:29], v[200:201]
	v_pk_mul_f32 v[30:31], v[30:31], v[202:203]
	v_cvt_pk_bf16_f32 v212, v24, v25
	v_cvt_pk_bf16_f32 v213, v26, v27
	v_cvt_pk_bf16_f32 v214, v28, v29
	v_cvt_pk_bf16_f32 v215, v30, v31
	s_add_u32 s20, s26, 0x3000
	s_addc_u32 s21, s27, 0
	global_store_dwordx4 v220, v[212:215], s[20:21] offset:2048
	s_waitcnt vmcnt(18)
	v_lshlrev_b32_e32 v180, 16, v60
	v_and_b32_e32 v181, 0xffff0000, v60
	v_lshlrev_b32_e32 v182, 16, v61
	v_and_b32_e32 v183, 0xffff0000, v61
	v_lshlrev_b32_e32 v184, 16, v62
	v_and_b32_e32 v185, 0xffff0000, v62
	v_lshlrev_b32_e32 v186, 16, v63
	v_and_b32_e32 v187, 0xffff0000, v63
	v_lshlrev_b32_e32 v188, 16, v64
	v_and_b32_e32 v189, 0xffff0000, v64
	v_lshlrev_b32_e32 v190, 16, v65
	v_and_b32_e32 v191, 0xffff0000, v65
	v_lshlrev_b32_e32 v192, 16, v66
	v_and_b32_e32 v193, 0xffff0000, v66
	v_lshlrev_b32_e32 v194, 16, v67
	v_and_b32_e32 v195, 0xffff0000, v67
	v_pk_mul_f32 v[0:1], v[180:181], v[188:189]
	v_pk_mul_f32 v[2:3], v[182:183], v[190:191]
	v_pk_mul_f32 v[4:5], v[184:185], v[192:193]
	v_pk_mul_f32 v[6:7], v[186:187], v[194:195]
	v_pk_mul_f32 v[24:25], v[92:93], v[8:9]
	v_pk_mul_f32 v[26:27], v[94:95], v[10:11]
	v_pk_mul_f32 v[28:29], v[96:97], v[12:13]
	v_pk_mul_f32 v[30:31], v[98:99], v[14:15]
	v_pk_fma_f32 v[24:25], v[100:101], v[16:17], v[24:25]
	v_pk_fma_f32 v[26:27], v[102:103], v[18:19], v[26:27]
	v_pk_fma_f32 v[28:29], v[104:105], v[20:21], v[28:29]
	v_pk_fma_f32 v[30:31], v[106:107], v[22:23], v[30:31]
	v_pk_fma_f32 v[24:25], v[108:109], v[0:1], v[24:25]
	v_pk_fma_f32 v[26:27], v[110:111], v[2:3], v[26:27]
	v_pk_fma_f32 v[28:29], v[112:113], v[4:5], v[28:29]
	v_pk_fma_f32 v[30:31], v[114:115], v[6:7], v[30:31]
	s_waitcnt vmcnt(35)
	v_lshlrev_b32_e32 v196, 16, v132
	v_and_b32_e32 v197, 0xffff0000, v132
	v_lshlrev_b32_e32 v198, 16, v133
	v_and_b32_e32 v199, 0xffff0000, v133
	v_lshlrev_b32_e32 v200, 16, v134
	v_and_b32_e32 v201, 0xffff0000, v134
	v_lshlrev_b32_e32 v202, 16, v135
	v_and_b32_e32 v203, 0xffff0000, v135
	v_pk_mul_f32 v[24:25], v[24:25], v[196:197]
	v_pk_mul_f32 v[26:27], v[26:27], v[198:199]
	v_pk_mul_f32 v[28:29], v[28:29], v[200:201]
	v_pk_mul_f32 v[30:31], v[30:31], v[202:203]
	v_cvt_pk_bf16_f32 v208, v24, v25
	v_cvt_pk_bf16_f32 v209, v26, v27
	v_cvt_pk_bf16_f32 v210, v28, v29
	v_cvt_pk_bf16_f32 v211, v30, v31
	s_add_u32 s20, s26, 0x4000
	s_addc_u32 s21, s27, 0
	global_store_dwordx4 v220, v[208:211], s[20:21] offset:2048
	s_waitcnt vmcnt(17)
	v_lshlrev_b32_e32 v180, 16, v68
	v_and_b32_e32 v181, 0xffff0000, v68
	v_lshlrev_b32_e32 v182, 16, v69
	v_and_b32_e32 v183, 0xffff0000, v69
	v_lshlrev_b32_e32 v184, 16, v70
	v_and_b32_e32 v185, 0xffff0000, v70
	v_lshlrev_b32_e32 v186, 16, v71
	v_and_b32_e32 v187, 0xffff0000, v71
	v_lshlrev_b32_e32 v188, 16, v72
	v_and_b32_e32 v189, 0xffff0000, v72
	v_lshlrev_b32_e32 v190, 16, v73
	v_and_b32_e32 v191, 0xffff0000, v73
	v_lshlrev_b32_e32 v192, 16, v74
	v_and_b32_e32 v193, 0xffff0000, v74
	v_lshlrev_b32_e32 v194, 16, v75
	v_and_b32_e32 v195, 0xffff0000, v75
	v_pk_mul_f32 v[8:9], v[180:181], v[188:189]
	v_pk_mul_f32 v[10:11], v[182:183], v[190:191]
	v_pk_mul_f32 v[12:13], v[184:185], v[192:193]
	v_pk_mul_f32 v[14:15], v[186:187], v[194:195]
	v_pk_mul_f32 v[24:25], v[92:93], v[16:17]
	v_pk_mul_f32 v[26:27], v[94:95], v[18:19]
	v_pk_mul_f32 v[28:29], v[96:97], v[20:21]
	v_pk_mul_f32 v[30:31], v[98:99], v[22:23]
	v_pk_fma_f32 v[24:25], v[100:101], v[0:1], v[24:25]
	v_pk_fma_f32 v[26:27], v[102:103], v[2:3], v[26:27]
	v_pk_fma_f32 v[28:29], v[104:105], v[4:5], v[28:29]
	v_pk_fma_f32 v[30:31], v[106:107], v[6:7], v[30:31]
	v_pk_fma_f32 v[24:25], v[108:109], v[8:9], v[24:25]
	v_pk_fma_f32 v[26:27], v[110:111], v[10:11], v[26:27]
	v_pk_fma_f32 v[28:29], v[112:113], v[12:13], v[28:29]
	v_pk_fma_f32 v[30:31], v[114:115], v[14:15], v[30:31]
	s_waitcnt vmcnt(35)
	v_lshlrev_b32_e32 v196, 16, v136
	v_and_b32_e32 v197, 0xffff0000, v136
	v_lshlrev_b32_e32 v198, 16, v137
	v_and_b32_e32 v199, 0xffff0000, v137
	v_lshlrev_b32_e32 v200, 16, v138
	v_and_b32_e32 v201, 0xffff0000, v138
	v_lshlrev_b32_e32 v202, 16, v139
	v_and_b32_e32 v203, 0xffff0000, v139
	v_pk_mul_f32 v[24:25], v[24:25], v[196:197]
	v_pk_mul_f32 v[26:27], v[26:27], v[198:199]
	v_pk_mul_f32 v[28:29], v[28:29], v[200:201]
	v_pk_mul_f32 v[30:31], v[30:31], v[202:203]
	v_cvt_pk_bf16_f32 v212, v24, v25
	v_cvt_pk_bf16_f32 v213, v26, v27
	v_cvt_pk_bf16_f32 v214, v28, v29
	v_cvt_pk_bf16_f32 v215, v30, v31
	s_add_u32 s20, s26, 0x5000
	s_addc_u32 s21, s27, 0
	global_store_dwordx4 v220, v[212:215], s[20:21] offset:2048
	s_waitcnt vmcnt(16)
	v_lshlrev_b32_e32 v180, 16, v76
	v_and_b32_e32 v181, 0xffff0000, v76
	v_lshlrev_b32_e32 v182, 16, v77
	v_and_b32_e32 v183, 0xffff0000, v77
	v_lshlrev_b32_e32 v184, 16, v78
	v_and_b32_e32 v185, 0xffff0000, v78
	v_lshlrev_b32_e32 v186, 16, v79
	v_and_b32_e32 v187, 0xffff0000, v79
	v_lshlrev_b32_e32 v188, 16, v80
	v_and_b32_e32 v189, 0xffff0000, v80
	v_lshlrev_b32_e32 v190, 16, v81
	v_and_b32_e32 v191, 0xffff0000, v81
	v_lshlrev_b32_e32 v192, 16, v82
	v_and_b32_e32 v193, 0xffff0000, v82
	v_lshlrev_b32_e32 v194, 16, v83
	v_and_b32_e32 v195, 0xffff0000, v83
	v_pk_mul_f32 v[16:17], v[180:181], v[188:189]
	v_pk_mul_f32 v[18:19], v[182:183], v[190:191]
	v_pk_mul_f32 v[20:21], v[184:185], v[192:193]
	v_pk_mul_f32 v[22:23], v[186:187], v[194:195]
	v_pk_mul_f32 v[24:25], v[92:93], v[0:1]
	v_pk_mul_f32 v[26:27], v[94:95], v[2:3]
	v_pk_mul_f32 v[28:29], v[96:97], v[4:5]
	v_pk_mul_f32 v[30:31], v[98:99], v[6:7]
	v_pk_fma_f32 v[24:25], v[100:101], v[8:9], v[24:25]
	v_pk_fma_f32 v[26:27], v[102:103], v[10:11], v[26:27]
	v_pk_fma_f32 v[28:29], v[104:105], v[12:13], v[28:29]
	v_pk_fma_f32 v[30:31], v[106:107], v[14:15], v[30:31]
	v_pk_fma_f32 v[24:25], v[108:109], v[16:17], v[24:25]
	v_pk_fma_f32 v[26:27], v[110:111], v[18:19], v[26:27]
	v_pk_fma_f32 v[28:29], v[112:113], v[20:21], v[28:29]
	v_pk_fma_f32 v[30:31], v[114:115], v[22:23], v[30:31]
	s_waitcnt vmcnt(35)
	v_lshlrev_b32_e32 v196, 16, v140
	v_and_b32_e32 v197, 0xffff0000, v140
	v_lshlrev_b32_e32 v198, 16, v141
	v_and_b32_e32 v199, 0xffff0000, v141
	v_lshlrev_b32_e32 v200, 16, v142
	v_and_b32_e32 v201, 0xffff0000, v142
	v_lshlrev_b32_e32 v202, 16, v143
	v_and_b32_e32 v203, 0xffff0000, v143
	v_pk_mul_f32 v[24:25], v[24:25], v[196:197]
	v_pk_mul_f32 v[26:27], v[26:27], v[198:199]
	v_pk_mul_f32 v[28:29], v[28:29], v[200:201]
	v_pk_mul_f32 v[30:31], v[30:31], v[202:203]
	v_cvt_pk_bf16_f32 v208, v24, v25
	v_cvt_pk_bf16_f32 v209, v26, v27
	v_cvt_pk_bf16_f32 v210, v28, v29
	v_cvt_pk_bf16_f32 v211, v30, v31
	s_add_u32 s20, s26, 0x6000
	s_addc_u32 s21, s27, 0
	global_store_dwordx4 v220, v[208:211], s[20:21] offset:2048
	s_waitcnt vmcnt(15)
	v_lshlrev_b32_e32 v180, 16, v84
	v_and_b32_e32 v181, 0xffff0000, v84
	v_lshlrev_b32_e32 v182, 16, v85
	v_and_b32_e32 v183, 0xffff0000, v85
	v_lshlrev_b32_e32 v184, 16, v86
	v_and_b32_e32 v185, 0xffff0000, v86
	v_lshlrev_b32_e32 v186, 16, v87
	v_and_b32_e32 v187, 0xffff0000, v87
	v_lshlrev_b32_e32 v188, 16, v88
	v_and_b32_e32 v189, 0xffff0000, v88
	v_lshlrev_b32_e32 v190, 16, v89
	v_and_b32_e32 v191, 0xffff0000, v89
	v_lshlrev_b32_e32 v192, 16, v90
	v_and_b32_e32 v193, 0xffff0000, v90
	v_lshlrev_b32_e32 v194, 16, v91
	v_and_b32_e32 v195, 0xffff0000, v91
	v_pk_mul_f32 v[0:1], v[180:181], v[188:189]
	v_pk_mul_f32 v[2:3], v[182:183], v[190:191]
	v_pk_mul_f32 v[4:5], v[184:185], v[192:193]
	v_pk_mul_f32 v[6:7], v[186:187], v[194:195]
	v_pk_mul_f32 v[24:25], v[92:93], v[8:9]
	v_pk_mul_f32 v[26:27], v[94:95], v[10:11]
	v_pk_mul_f32 v[28:29], v[96:97], v[12:13]
	v_pk_mul_f32 v[30:31], v[98:99], v[14:15]
	v_pk_fma_f32 v[24:25], v[100:101], v[16:17], v[24:25]
	v_pk_fma_f32 v[26:27], v[102:103], v[18:19], v[26:27]
	v_pk_fma_f32 v[28:29], v[104:105], v[20:21], v[28:29]
	v_pk_fma_f32 v[30:31], v[106:107], v[22:23], v[30:31]
	v_pk_fma_f32 v[24:25], v[108:109], v[0:1], v[24:25]
	v_pk_fma_f32 v[26:27], v[110:111], v[2:3], v[26:27]
	v_pk_fma_f32 v[28:29], v[112:113], v[4:5], v[28:29]
	v_pk_fma_f32 v[30:31], v[114:115], v[6:7], v[30:31]
	s_waitcnt vmcnt(35)
	v_lshlrev_b32_e32 v196, 16, v144
	v_and_b32_e32 v197, 0xffff0000, v144
	v_lshlrev_b32_e32 v198, 16, v145
	v_and_b32_e32 v199, 0xffff0000, v145
	v_lshlrev_b32_e32 v200, 16, v146
	v_and_b32_e32 v201, 0xffff0000, v146
	v_lshlrev_b32_e32 v202, 16, v147
	v_and_b32_e32 v203, 0xffff0000, v147
	v_pk_mul_f32 v[24:25], v[24:25], v[196:197]
	v_pk_mul_f32 v[26:27], v[26:27], v[198:199]
	v_pk_mul_f32 v[28:29], v[28:29], v[200:201]
	v_pk_mul_f32 v[30:31], v[30:31], v[202:203]
	v_cvt_pk_bf16_f32 v212, v24, v25
	v_cvt_pk_bf16_f32 v213, v26, v27
	v_cvt_pk_bf16_f32 v214, v28, v29
	v_cvt_pk_bf16_f32 v215, v30, v31
	s_add_u32 s20, s26, 0x7000
	s_addc_u32 s21, s27, 0
	global_store_dwordx4 v220, v[212:215], s[20:21] offset:2048
